# PEER u-side: 6 table rows in flight per wave instead of 4 (24 loads outstanding, extra row buffers in v196-v227)
# speedup vs baseline: 1.0049x; 1.0049x over previous
.LBB0_1473:
	s_or_b64 exec, exec, s[30:31]
	s_mov_b32 s31, 0
	v_readlane_b32 s30, v76, 0
	s_lshl_b32 s30, s30, 12
	v_lshl_add_u64 v[194:195], v[86:87], 0, s[30:31]
	global_load_dwordx4 v[10:13], v[194:195], off
	global_load_dwordx4 v[14:17], v[194:195], off offset:1024
	global_load_dwordx4 v[18:21], v[194:195], off offset:2048
	global_load_dwordx4 v[22:25], v[194:195], off offset:3072
	v_readlane_b32 s30, v76, 1
	s_lshl_b32 s30, s30, 12
	v_lshl_add_u64 v[194:195], v[86:87], 0, s[30:31]
	global_load_dwordx4 v[26:29], v[194:195], off
	global_load_dwordx4 v[30:33], v[194:195], off offset:1024
	global_load_dwordx4 v[34:37], v[194:195], off offset:2048
	global_load_dwordx4 v[38:41], v[194:195], off offset:3072
	v_readlane_b32 s30, v76, 2
	s_lshl_b32 s30, s30, 12
	v_lshl_add_u64 v[194:195], v[86:87], 0, s[30:31]
	global_load_dwordx4 v[42:45], v[194:195], off
	global_load_dwordx4 v[46:49], v[194:195], off offset:1024
	global_load_dwordx4 v[50:53], v[194:195], off offset:2048
	global_load_dwordx4 v[54:57], v[194:195], off offset:3072
	v_readlane_b32 s30, v76, 3
	s_lshl_b32 s30, s30, 12
	v_lshl_add_u64 v[194:195], v[86:87], 0, s[30:31]
	global_load_dwordx4 v[58:61], v[194:195], off
	global_load_dwordx4 v[62:65], v[194:195], off offset:1024
	global_load_dwordx4 v[66:69], v[194:195], off offset:2048
	global_load_dwordx4 v[70:73], v[194:195], off offset:3072
	v_readlane_b32 s30, v76, 4
	s_lshl_b32 s30, s30, 12
	v_lshl_add_u64 v[194:195], v[86:87], 0, s[30:31]
	global_load_dwordx4 v[196:199], v[194:195], off
	global_load_dwordx4 v[200:203], v[194:195], off offset:1024
	global_load_dwordx4 v[204:207], v[194:195], off offset:2048
	global_load_dwordx4 v[208:211], v[194:195], off offset:3072
	v_readlane_b32 s30, v76, 5
	s_lshl_b32 s30, s30, 12
	v_lshl_add_u64 v[194:195], v[86:87], 0, s[30:31]
	global_load_dwordx4 v[212:215], v[194:195], off
	global_load_dwordx4 v[216:219], v[194:195], off offset:1024
	global_load_dwordx4 v[220:223], v[194:195], off offset:2048
	global_load_dwordx4 v[224:227], v[194:195], off offset:3072
	v_readlane_b32 s30, v76, 6
	s_lshl_b32 s30, s30, 12
	v_lshl_add_u64 v[194:195], v[86:87], 0, s[30:31]
	s_waitcnt vmcnt(23)
	v_cvt_f32_ubyte0_e32 v240, v10
	v_cvt_f32_ubyte1_e32 v241, v10
	v_cvt_f32_ubyte2_e32 v242, v10
	v_cvt_f32_ubyte3_e32 v243, v10
	v_cvt_f32_ubyte0_e32 v244, v11
	v_cvt_f32_ubyte1_e32 v245, v11
	v_cvt_f32_ubyte2_e32 v246, v11
	v_cvt_f32_ubyte3_e32 v247, v11
	v_pk_mul_f32 v[248:249], v[240:241], v[162:163]
	v_pk_mul_f32 v[250:251], v[242:243], v[160:161]
	v_cvt_f32_ubyte0_e32 v240, v12
	v_cvt_f32_ubyte1_e32 v241, v12
	v_cvt_f32_ubyte2_e32 v242, v12
	v_cvt_f32_ubyte3_e32 v243, v12
	v_pk_fma_f32 v[248:249], v[244:245], v[158:159], v[248:249]
	v_pk_fma_f32 v[250:251], v[246:247], v[148:149], v[250:251]
	v_cvt_f32_ubyte0_e32 v244, v13
	v_cvt_f32_ubyte1_e32 v245, v13
	v_cvt_f32_ubyte2_e32 v246, v13
	v_cvt_f32_ubyte3_e32 v247, v13
	global_load_dwordx4 v[10:13], v[194:195], off
	v_pk_fma_f32 v[248:249], v[240:241], v[140:141], v[248:249]
	v_pk_fma_f32 v[250:251], v[242:243], v[128:129], v[250:251]
	s_waitcnt vmcnt(23)
	v_cvt_f32_ubyte0_e32 v240, v14
	v_cvt_f32_ubyte1_e32 v241, v14
	v_cvt_f32_ubyte2_e32 v242, v14
	v_cvt_f32_ubyte3_e32 v243, v14
	v_pk_fma_f32 v[248:249], v[244:245], v[120:121], v[248:249]
	v_pk_fma_f32 v[250:251], v[246:247], v[112:113], v[250:251]
	v_cvt_f32_ubyte0_e32 v244, v15
	v_cvt_f32_ubyte1_e32 v245, v15
	v_cvt_f32_ubyte2_e32 v246, v15
	v_cvt_f32_ubyte3_e32 v247, v15
	v_pk_fma_f32 v[248:249], v[240:241], v[106:107], v[248:249]
	v_pk_fma_f32 v[250:251], v[242:243], v[102:103], v[250:251]
	v_cvt_f32_ubyte0_e32 v240, v16
	v_cvt_f32_ubyte1_e32 v241, v16
	v_cvt_f32_ubyte2_e32 v242, v16
	v_cvt_f32_ubyte3_e32 v243, v16
	v_pk_fma_f32 v[248:249], v[244:245], v[152:153], v[248:249]
	v_pk_fma_f32 v[250:251], v[246:247], v[100:101], v[250:251]
	v_cvt_f32_ubyte0_e32 v244, v17
	v_cvt_f32_ubyte1_e32 v245, v17
	v_cvt_f32_ubyte2_e32 v246, v17
	v_cvt_f32_ubyte3_e32 v247, v17
	global_load_dwordx4 v[14:17], v[194:195], off offset:1024
	v_pk_fma_f32 v[248:249], v[240:241], v[136:137], v[248:249]
	v_pk_fma_f32 v[250:251], v[242:243], v[122:123], v[250:251]
	s_waitcnt vmcnt(23)
	v_cvt_f32_ubyte0_e32 v240, v18
	v_cvt_f32_ubyte1_e32 v241, v18
	v_cvt_f32_ubyte2_e32 v242, v18
	v_cvt_f32_ubyte3_e32 v243, v18
	v_pk_fma_f32 v[248:249], v[244:245], v[116:117], v[248:249]
	v_pk_fma_f32 v[250:251], v[246:247], v[110:111], v[250:251]
	v_cvt_f32_ubyte0_e32 v244, v19
	v_cvt_f32_ubyte1_e32 v245, v19
	v_cvt_f32_ubyte2_e32 v246, v19
	v_cvt_f32_ubyte3_e32 v247, v19
	v_pk_fma_f32 v[248:249], v[240:241], v[156:157], v[248:249]
	v_pk_fma_f32 v[250:251], v[242:243], v[146:147], v[250:251]
	v_cvt_f32_ubyte0_e32 v240, v20
	v_cvt_f32_ubyte1_e32 v241, v20
	v_cvt_f32_ubyte2_e32 v242, v20
	v_cvt_f32_ubyte3_e32 v243, v20
	v_pk_fma_f32 v[248:249], v[244:245], v[142:143], v[248:249]
	v_pk_fma_f32 v[250:251], v[246:247], v[130:131], v[250:251]
	v_cvt_f32_ubyte0_e32 v244, v21
	v_cvt_f32_ubyte1_e32 v245, v21
	v_cvt_f32_ubyte2_e32 v246, v21
	v_cvt_f32_ubyte3_e32 v247, v21
	global_load_dwordx4 v[18:21], v[194:195], off offset:2048
	v_pk_fma_f32 v[248:249], v[240:241], v[124:125], v[248:249]
	v_pk_fma_f32 v[250:251], v[242:243], v[114:115], v[250:251]
	s_waitcnt vmcnt(23)
	v_cvt_f32_ubyte0_e32 v240, v22
	v_cvt_f32_ubyte1_e32 v241, v22
	v_cvt_f32_ubyte2_e32 v242, v22
	v_cvt_f32_ubyte3_e32 v243, v22
	v_pk_fma_f32 v[248:249], v[244:245], v[108:109], v[248:249]
	v_pk_fma_f32 v[250:251], v[246:247], v[104:105], v[250:251]
	v_cvt_f32_ubyte0_e32 v244, v23
	v_cvt_f32_ubyte1_e32 v245, v23
	v_cvt_f32_ubyte2_e32 v246, v23
	v_cvt_f32_ubyte3_e32 v247, v23
	v_pk_fma_f32 v[248:249], v[240:241], v[154:155], v[248:249]
	v_pk_fma_f32 v[250:251], v[242:243], v[138:139], v[250:251]
	v_cvt_f32_ubyte0_e32 v240, v24
	v_cvt_f32_ubyte1_e32 v241, v24
	v_cvt_f32_ubyte2_e32 v242, v24
	v_cvt_f32_ubyte3_e32 v243, v24
	v_pk_fma_f32 v[248:249], v[244:245], v[150:151], v[248:249]
	v_pk_fma_f32 v[250:251], v[246:247], v[132:133], v[250:251]
	v_cvt_f32_ubyte0_e32 v244, v25
	v_cvt_f32_ubyte1_e32 v245, v25
	v_cvt_f32_ubyte2_e32 v246, v25
	v_cvt_f32_ubyte3_e32 v247, v25
	global_load_dwordx4 v[22:25], v[194:195], off offset:3072
	v_pk_fma_f32 v[248:249], v[240:241], v[144:145], v[248:249]
	v_pk_fma_f32 v[250:251], v[242:243], v[126:127], v[250:251]
	v_readlane_b32 s30, v76, 7
	s_lshl_b32 s30, s30, 12
	v_lshl_add_u64 v[194:195], v[86:87], 0, s[30:31]
	s_waitcnt vmcnt(23)
	v_cvt_f32_ubyte0_e32 v240, v26
	v_cvt_f32_ubyte1_e32 v241, v26
	v_cvt_f32_ubyte2_e32 v242, v26
	v_cvt_f32_ubyte3_e32 v243, v26
	v_pk_fma_f32 v[248:249], v[244:245], v[134:135], v[248:249]
	v_pk_fma_f32 v[250:251], v[246:247], v[118:119], v[250:251]
	v_cvt_f32_ubyte0_e32 v244, v27
	v_cvt_f32_ubyte1_e32 v245, v27
	v_cvt_f32_ubyte2_e32 v246, v27
	v_cvt_f32_ubyte3_e32 v247, v27
	v_pk_add_f32 v[252:253], v[248:249], v[250:251]
	v_pk_mul_f32 v[248:249], v[240:241], v[162:163]
	v_pk_mul_f32 v[250:251], v[242:243], v[160:161]
	v_cvt_f32_ubyte0_e32 v240, v28
	v_cvt_f32_ubyte1_e32 v241, v28
	v_cvt_f32_ubyte2_e32 v242, v28
	v_cvt_f32_ubyte3_e32 v243, v28
	v_pk_fma_f32 v[248:249], v[244:245], v[158:159], v[248:249]
	v_pk_fma_f32 v[250:251], v[246:247], v[148:149], v[250:251]
	v_add_f32_e32 v178, v252, v253
	v_cvt_f32_ubyte0_e32 v244, v29
	v_cvt_f32_ubyte1_e32 v245, v29
	v_cvt_f32_ubyte2_e32 v246, v29
	v_cvt_f32_ubyte3_e32 v247, v29
	global_load_dwordx4 v[26:29], v[194:195], off
	v_pk_fma_f32 v[248:249], v[240:241], v[140:141], v[248:249]
	v_pk_fma_f32 v[250:251], v[242:243], v[128:129], v[250:251]
	s_waitcnt vmcnt(23)
	v_cvt_f32_ubyte0_e32 v240, v30
	v_cvt_f32_ubyte1_e32 v241, v30
	v_cvt_f32_ubyte2_e32 v242, v30
	v_cvt_f32_ubyte3_e32 v243, v30
	v_pk_fma_f32 v[248:249], v[244:245], v[120:121], v[248:249]
	v_pk_fma_f32 v[250:251], v[246:247], v[112:113], v[250:251]
	v_cvt_f32_ubyte0_e32 v244, v31
	v_cvt_f32_ubyte1_e32 v245, v31
	v_cvt_f32_ubyte2_e32 v246, v31
	v_cvt_f32_ubyte3_e32 v247, v31
	v_pk_fma_f32 v[248:249], v[240:241], v[106:107], v[248:249]
	v_pk_fma_f32 v[250:251], v[242:243], v[102:103], v[250:251]
	v_cvt_f32_ubyte0_e32 v240, v32
	v_cvt_f32_ubyte1_e32 v241, v32
	v_cvt_f32_ubyte2_e32 v242, v32
	v_cvt_f32_ubyte3_e32 v243, v32
	v_pk_fma_f32 v[248:249], v[244:245], v[152:153], v[248:249]
	v_pk_fma_f32 v[250:251], v[246:247], v[100:101], v[250:251]
	v_cvt_f32_ubyte0_e32 v244, v33
	v_cvt_f32_ubyte1_e32 v245, v33
	v_cvt_f32_ubyte2_e32 v246, v33
	v_cvt_f32_ubyte3_e32 v247, v33
	global_load_dwordx4 v[30:33], v[194:195], off offset:1024
	v_pk_fma_f32 v[248:249], v[240:241], v[136:137], v[248:249]
	v_pk_fma_f32 v[250:251], v[242:243], v[122:123], v[250:251]
	s_waitcnt vmcnt(23)
	v_cvt_f32_ubyte0_e32 v240, v34
	v_cvt_f32_ubyte1_e32 v241, v34
	v_cvt_f32_ubyte2_e32 v242, v34
	v_cvt_f32_ubyte3_e32 v243, v34
	v_pk_fma_f32 v[248:249], v[244:245], v[116:117], v[248:249]
	v_pk_fma_f32 v[250:251], v[246:247], v[110:111], v[250:251]
	v_cvt_f32_ubyte0_e32 v244, v35
	v_cvt_f32_ubyte1_e32 v245, v35
	v_cvt_f32_ubyte2_e32 v246, v35
	v_cvt_f32_ubyte3_e32 v247, v35
	v_pk_fma_f32 v[248:249], v[240:241], v[156:157], v[248:249]
	v_pk_fma_f32 v[250:251], v[242:243], v[146:147], v[250:251]
	v_cvt_f32_ubyte0_e32 v240, v36
	v_cvt_f32_ubyte1_e32 v241, v36
	v_cvt_f32_ubyte2_e32 v242, v36
	v_cvt_f32_ubyte3_e32 v243, v36
	v_pk_fma_f32 v[248:249], v[244:245], v[142:143], v[248:249]
	v_pk_fma_f32 v[250:251], v[246:247], v[130:131], v[250:251]
	v_cvt_f32_ubyte0_e32 v244, v37
	v_cvt_f32_ubyte1_e32 v245, v37
	v_cvt_f32_ubyte2_e32 v246, v37
	v_cvt_f32_ubyte3_e32 v247, v37
	global_load_dwordx4 v[34:37], v[194:195], off offset:2048
	v_pk_fma_f32 v[248:249], v[240:241], v[124:125], v[248:249]
	v_pk_fma_f32 v[250:251], v[242:243], v[114:115], v[250:251]
	s_waitcnt vmcnt(23)
	v_cvt_f32_ubyte0_e32 v240, v38
	v_cvt_f32_ubyte1_e32 v241, v38
	v_cvt_f32_ubyte2_e32 v242, v38
	v_cvt_f32_ubyte3_e32 v243, v38
	v_pk_fma_f32 v[248:249], v[244:245], v[108:109], v[248:249]
	v_pk_fma_f32 v[250:251], v[246:247], v[104:105], v[250:251]
	v_cvt_f32_ubyte0_e32 v244, v39
	v_cvt_f32_ubyte1_e32 v245, v39
	v_cvt_f32_ubyte2_e32 v246, v39
	v_cvt_f32_ubyte3_e32 v247, v39
	v_pk_fma_f32 v[248:249], v[240:241], v[154:155], v[248:249]
	v_pk_fma_f32 v[250:251], v[242:243], v[138:139], v[250:251]
	v_cvt_f32_ubyte0_e32 v240, v40
	v_cvt_f32_ubyte1_e32 v241, v40
	v_cvt_f32_ubyte2_e32 v242, v40
	v_cvt_f32_ubyte3_e32 v243, v40
	v_pk_fma_f32 v[248:249], v[244:245], v[150:151], v[248:249]
	v_pk_fma_f32 v[250:251], v[246:247], v[132:133], v[250:251]
	v_cvt_f32_ubyte0_e32 v244, v41
	v_cvt_f32_ubyte1_e32 v245, v41
	v_cvt_f32_ubyte2_e32 v246, v41
	v_cvt_f32_ubyte3_e32 v247, v41
	global_load_dwordx4 v[38:41], v[194:195], off offset:3072
	v_pk_fma_f32 v[248:249], v[240:241], v[144:145], v[248:249]
	v_pk_fma_f32 v[250:251], v[242:243], v[126:127], v[250:251]
	v_readlane_b32 s30, v76, 8
	s_lshl_b32 s30, s30, 12
	v_lshl_add_u64 v[194:195], v[86:87], 0, s[30:31]
	s_waitcnt vmcnt(23)
	v_cvt_f32_ubyte0_e32 v240, v42
	v_cvt_f32_ubyte1_e32 v241, v42
	v_cvt_f32_ubyte2_e32 v242, v42
	v_cvt_f32_ubyte3_e32 v243, v42
	v_pk_fma_f32 v[248:249], v[244:245], v[134:135], v[248:249]
	v_pk_fma_f32 v[250:251], v[246:247], v[118:119], v[250:251]
	v_cvt_f32_ubyte0_e32 v244, v43
	v_cvt_f32_ubyte1_e32 v245, v43
	v_cvt_f32_ubyte2_e32 v246, v43
	v_cvt_f32_ubyte3_e32 v247, v43
	v_pk_add_f32 v[252:253], v[248:249], v[250:251]
	v_pk_mul_f32 v[248:249], v[240:241], v[162:163]
	v_pk_mul_f32 v[250:251], v[242:243], v[160:161]
	v_cvt_f32_ubyte0_e32 v240, v44
	v_cvt_f32_ubyte1_e32 v241, v44
	v_cvt_f32_ubyte2_e32 v242, v44
	v_cvt_f32_ubyte3_e32 v243, v44
	v_pk_fma_f32 v[248:249], v[244:245], v[158:159], v[248:249]
	v_pk_fma_f32 v[250:251], v[246:247], v[148:149], v[250:251]
	v_add_f32_e32 v179, v252, v253
	v_cvt_f32_ubyte0_e32 v244, v45
	v_cvt_f32_ubyte1_e32 v245, v45
	v_cvt_f32_ubyte2_e32 v246, v45
	v_cvt_f32_ubyte3_e32 v247, v45
	global_load_dwordx4 v[42:45], v[194:195], off
	v_pk_fma_f32 v[248:249], v[240:241], v[140:141], v[248:249]
	v_pk_fma_f32 v[250:251], v[242:243], v[128:129], v[250:251]
	s_waitcnt vmcnt(23)
	v_cvt_f32_ubyte0_e32 v240, v46
	v_cvt_f32_ubyte1_e32 v241, v46
	v_cvt_f32_ubyte2_e32 v242, v46
	v_cvt_f32_ubyte3_e32 v243, v46
	v_pk_fma_f32 v[248:249], v[244:245], v[120:121], v[248:249]
	v_pk_fma_f32 v[250:251], v[246:247], v[112:113], v[250:251]
	v_cvt_f32_ubyte0_e32 v244, v47
	v_cvt_f32_ubyte1_e32 v245, v47
	v_cvt_f32_ubyte2_e32 v246, v47
	v_cvt_f32_ubyte3_e32 v247, v47
	v_pk_fma_f32 v[248:249], v[240:241], v[106:107], v[248:249]
	v_pk_fma_f32 v[250:251], v[242:243], v[102:103], v[250:251]
	v_cvt_f32_ubyte0_e32 v240, v48
	v_cvt_f32_ubyte1_e32 v241, v48
	v_cvt_f32_ubyte2_e32 v242, v48
	v_cvt_f32_ubyte3_e32 v243, v48
	v_pk_fma_f32 v[248:249], v[244:245], v[152:153], v[248:249]
	v_pk_fma_f32 v[250:251], v[246:247], v[100:101], v[250:251]
	v_cvt_f32_ubyte0_e32 v244, v49
	v_cvt_f32_ubyte1_e32 v245, v49
	v_cvt_f32_ubyte2_e32 v246, v49
	v_cvt_f32_ubyte3_e32 v247, v49
	global_load_dwordx4 v[46:49], v[194:195], off offset:1024
	v_pk_fma_f32 v[248:249], v[240:241], v[136:137], v[248:249]
	v_pk_fma_f32 v[250:251], v[242:243], v[122:123], v[250:251]
	s_waitcnt vmcnt(23)
	v_cvt_f32_ubyte0_e32 v240, v50
	v_cvt_f32_ubyte1_e32 v241, v50
	v_cvt_f32_ubyte2_e32 v242, v50
	v_cvt_f32_ubyte3_e32 v243, v50
	v_pk_fma_f32 v[248:249], v[244:245], v[116:117], v[248:249]
	v_pk_fma_f32 v[250:251], v[246:247], v[110:111], v[250:251]
	v_cvt_f32_ubyte0_e32 v244, v51
	v_cvt_f32_ubyte1_e32 v245, v51
	v_cvt_f32_ubyte2_e32 v246, v51
	v_cvt_f32_ubyte3_e32 v247, v51
	v_pk_fma_f32 v[248:249], v[240:241], v[156:157], v[248:249]
	v_pk_fma_f32 v[250:251], v[242:243], v[146:147], v[250:251]
	v_cvt_f32_ubyte0_e32 v240, v52
	v_cvt_f32_ubyte1_e32 v241, v52
	v_cvt_f32_ubyte2_e32 v242, v52
	v_cvt_f32_ubyte3_e32 v243, v52
	v_pk_fma_f32 v[248:249], v[244:245], v[142:143], v[248:249]
	v_pk_fma_f32 v[250:251], v[246:247], v[130:131], v[250:251]
	v_cvt_f32_ubyte0_e32 v244, v53
	v_cvt_f32_ubyte1_e32 v245, v53
	v_cvt_f32_ubyte2_e32 v246, v53
	v_cvt_f32_ubyte3_e32 v247, v53
	global_load_dwordx4 v[50:53], v[194:195], off offset:2048
	v_pk_fma_f32 v[248:249], v[240:241], v[124:125], v[248:249]
	v_pk_fma_f32 v[250:251], v[242:243], v[114:115], v[250:251]
	s_waitcnt vmcnt(23)
	v_cvt_f32_ubyte0_e32 v240, v54
	v_cvt_f32_ubyte1_e32 v241, v54
	v_cvt_f32_ubyte2_e32 v242, v54
	v_cvt_f32_ubyte3_e32 v243, v54
	v_pk_fma_f32 v[248:249], v[244:245], v[108:109], v[248:249]
	v_pk_fma_f32 v[250:251], v[246:247], v[104:105], v[250:251]
	v_cvt_f32_ubyte0_e32 v244, v55
	v_cvt_f32_ubyte1_e32 v245, v55
	v_cvt_f32_ubyte2_e32 v246, v55
	v_cvt_f32_ubyte3_e32 v247, v55
	v_pk_fma_f32 v[248:249], v[240:241], v[154:155], v[248:249]
	v_pk_fma_f32 v[250:251], v[242:243], v[138:139], v[250:251]
	v_cvt_f32_ubyte0_e32 v240, v56
	v_cvt_f32_ubyte1_e32 v241, v56
	v_cvt_f32_ubyte2_e32 v242, v56
	v_cvt_f32_ubyte3_e32 v243, v56
	v_pk_fma_f32 v[248:249], v[244:245], v[150:151], v[248:249]
	v_pk_fma_f32 v[250:251], v[246:247], v[132:133], v[250:251]
	v_cvt_f32_ubyte0_e32 v244, v57
	v_cvt_f32_ubyte1_e32 v245, v57
	v_cvt_f32_ubyte2_e32 v246, v57
	v_cvt_f32_ubyte3_e32 v247, v57
	global_load_dwordx4 v[54:57], v[194:195], off offset:3072
	v_pk_fma_f32 v[248:249], v[240:241], v[144:145], v[248:249]
	v_pk_fma_f32 v[250:251], v[242:243], v[126:127], v[250:251]
	v_readlane_b32 s30, v76, 9
	s_lshl_b32 s30, s30, 12
	v_lshl_add_u64 v[194:195], v[86:87], 0, s[30:31]
	s_waitcnt vmcnt(23)
	v_cvt_f32_ubyte0_e32 v240, v58
	v_cvt_f32_ubyte1_e32 v241, v58
	v_cvt_f32_ubyte2_e32 v242, v58
	v_cvt_f32_ubyte3_e32 v243, v58
	v_pk_fma_f32 v[248:249], v[244:245], v[134:135], v[248:249]
	v_pk_fma_f32 v[250:251], v[246:247], v[118:119], v[250:251]
	v_cvt_f32_ubyte0_e32 v244, v59
	v_cvt_f32_ubyte1_e32 v245, v59
	v_cvt_f32_ubyte2_e32 v246, v59
	v_cvt_f32_ubyte3_e32 v247, v59
	v_pk_add_f32 v[252:253], v[248:249], v[250:251]
	v_pk_mul_f32 v[248:249], v[240:241], v[162:163]
	v_pk_mul_f32 v[250:251], v[242:243], v[160:161]
	v_cvt_f32_ubyte0_e32 v240, v60
	v_cvt_f32_ubyte1_e32 v241, v60
	v_cvt_f32_ubyte2_e32 v242, v60
	v_cvt_f32_ubyte3_e32 v243, v60
	v_pk_fma_f32 v[248:249], v[244:245], v[158:159], v[248:249]
	v_pk_fma_f32 v[250:251], v[246:247], v[148:149], v[250:251]
	v_add_f32_e32 v180, v252, v253
	v_cvt_f32_ubyte0_e32 v244, v61
	v_cvt_f32_ubyte1_e32 v245, v61
	v_cvt_f32_ubyte2_e32 v246, v61
	v_cvt_f32_ubyte3_e32 v247, v61
	global_load_dwordx4 v[58:61], v[194:195], off
	v_pk_fma_f32 v[248:249], v[240:241], v[140:141], v[248:249]
	v_pk_fma_f32 v[250:251], v[242:243], v[128:129], v[250:251]
	s_waitcnt vmcnt(23)
	v_cvt_f32_ubyte0_e32 v240, v62
	v_cvt_f32_ubyte1_e32 v241, v62
	v_cvt_f32_ubyte2_e32 v242, v62
	v_cvt_f32_ubyte3_e32 v243, v62
	v_pk_fma_f32 v[248:249], v[244:245], v[120:121], v[248:249]
	v_pk_fma_f32 v[250:251], v[246:247], v[112:113], v[250:251]
	v_cvt_f32_ubyte0_e32 v244, v63
	v_cvt_f32_ubyte1_e32 v245, v63
	v_cvt_f32_ubyte2_e32 v246, v63
	v_cvt_f32_ubyte3_e32 v247, v63
	v_pk_fma_f32 v[248:249], v[240:241], v[106:107], v[248:249]
	v_pk_fma_f32 v[250:251], v[242:243], v[102:103], v[250:251]
	v_cvt_f32_ubyte0_e32 v240, v64
	v_cvt_f32_ubyte1_e32 v241, v64
	v_cvt_f32_ubyte2_e32 v242, v64
	v_cvt_f32_ubyte3_e32 v243, v64
	v_pk_fma_f32 v[248:249], v[244:245], v[152:153], v[248:249]
	v_pk_fma_f32 v[250:251], v[246:247], v[100:101], v[250:251]
	v_cvt_f32_ubyte0_e32 v244, v65
	v_cvt_f32_ubyte1_e32 v245, v65
	v_cvt_f32_ubyte2_e32 v246, v65
	v_cvt_f32_ubyte3_e32 v247, v65
	global_load_dwordx4 v[62:65], v[194:195], off offset:1024
	v_pk_fma_f32 v[248:249], v[240:241], v[136:137], v[248:249]
	v_pk_fma_f32 v[250:251], v[242:243], v[122:123], v[250:251]
	s_waitcnt vmcnt(23)
	v_cvt_f32_ubyte0_e32 v240, v66
	v_cvt_f32_ubyte1_e32 v241, v66
	v_cvt_f32_ubyte2_e32 v242, v66
	v_cvt_f32_ubyte3_e32 v243, v66
	v_pk_fma_f32 v[248:249], v[244:245], v[116:117], v[248:249]
	v_pk_fma_f32 v[250:251], v[246:247], v[110:111], v[250:251]
	v_cvt_f32_ubyte0_e32 v244, v67
	v_cvt_f32_ubyte1_e32 v245, v67
	v_cvt_f32_ubyte2_e32 v246, v67
	v_cvt_f32_ubyte3_e32 v247, v67
	v_pk_fma_f32 v[248:249], v[240:241], v[156:157], v[248:249]
	v_pk_fma_f32 v[250:251], v[242:243], v[146:147], v[250:251]
	v_cvt_f32_ubyte0_e32 v240, v68
	v_cvt_f32_ubyte1_e32 v241, v68
	v_cvt_f32_ubyte2_e32 v242, v68
	v_cvt_f32_ubyte3_e32 v243, v68
	v_pk_fma_f32 v[248:249], v[244:245], v[142:143], v[248:249]
	v_pk_fma_f32 v[250:251], v[246:247], v[130:131], v[250:251]
	v_cvt_f32_ubyte0_e32 v244, v69
	v_cvt_f32_ubyte1_e32 v245, v69
	v_cvt_f32_ubyte2_e32 v246, v69
	v_cvt_f32_ubyte3_e32 v247, v69
	global_load_dwordx4 v[66:69], v[194:195], off offset:2048
	v_pk_fma_f32 v[248:249], v[240:241], v[124:125], v[248:249]
	v_pk_fma_f32 v[250:251], v[242:243], v[114:115], v[250:251]
	s_waitcnt vmcnt(23)
	v_cvt_f32_ubyte0_e32 v240, v70
	v_cvt_f32_ubyte1_e32 v241, v70
	v_cvt_f32_ubyte2_e32 v242, v70
	v_cvt_f32_ubyte3_e32 v243, v70
	v_pk_fma_f32 v[248:249], v[244:245], v[108:109], v[248:249]
	v_pk_fma_f32 v[250:251], v[246:247], v[104:105], v[250:251]
	v_cvt_f32_ubyte0_e32 v244, v71
	v_cvt_f32_ubyte1_e32 v245, v71
	v_cvt_f32_ubyte2_e32 v246, v71
	v_cvt_f32_ubyte3_e32 v247, v71
	v_pk_fma_f32 v[248:249], v[240:241], v[154:155], v[248:249]
	v_pk_fma_f32 v[250:251], v[242:243], v[138:139], v[250:251]
	v_cvt_f32_ubyte0_e32 v240, v72
	v_cvt_f32_ubyte1_e32 v241, v72
	v_cvt_f32_ubyte2_e32 v242, v72
	v_cvt_f32_ubyte3_e32 v243, v72
	v_pk_fma_f32 v[248:249], v[244:245], v[150:151], v[248:249]
	v_pk_fma_f32 v[250:251], v[246:247], v[132:133], v[250:251]
	v_cvt_f32_ubyte0_e32 v244, v73
	v_cvt_f32_ubyte1_e32 v245, v73
	v_cvt_f32_ubyte2_e32 v246, v73
	v_cvt_f32_ubyte3_e32 v247, v73
	global_load_dwordx4 v[70:73], v[194:195], off offset:3072
	v_pk_fma_f32 v[248:249], v[240:241], v[144:145], v[248:249]
	v_pk_fma_f32 v[250:251], v[242:243], v[126:127], v[250:251]
	v_readlane_b32 s30, v76, 10
	s_lshl_b32 s30, s30, 12
	v_lshl_add_u64 v[194:195], v[86:87], 0, s[30:31]
	s_waitcnt vmcnt(23)
	v_cvt_f32_ubyte0_e32 v240, v196
	v_cvt_f32_ubyte1_e32 v241, v196
	v_cvt_f32_ubyte2_e32 v242, v196
	v_cvt_f32_ubyte3_e32 v243, v196
	v_pk_fma_f32 v[248:249], v[244:245], v[134:135], v[248:249]
	v_pk_fma_f32 v[250:251], v[246:247], v[118:119], v[250:251]
	v_cvt_f32_ubyte0_e32 v244, v197
	v_cvt_f32_ubyte1_e32 v245, v197
	v_cvt_f32_ubyte2_e32 v246, v197
	v_cvt_f32_ubyte3_e32 v247, v197
	v_pk_add_f32 v[252:253], v[248:249], v[250:251]
	v_pk_mul_f32 v[248:249], v[240:241], v[162:163]
	v_pk_mul_f32 v[250:251], v[242:243], v[160:161]
	v_cvt_f32_ubyte0_e32 v240, v198
	v_cvt_f32_ubyte1_e32 v241, v198
	v_cvt_f32_ubyte2_e32 v242, v198
	v_cvt_f32_ubyte3_e32 v243, v198
	v_pk_fma_f32 v[248:249], v[244:245], v[158:159], v[248:249]
	v_pk_fma_f32 v[250:251], v[246:247], v[148:149], v[250:251]
	v_add_f32_e32 v181, v252, v253
	v_cvt_f32_ubyte0_e32 v244, v199
	v_cvt_f32_ubyte1_e32 v245, v199
	v_cvt_f32_ubyte2_e32 v246, v199
	v_cvt_f32_ubyte3_e32 v247, v199
	global_load_dwordx4 v[196:199], v[194:195], off
	v_pk_fma_f32 v[248:249], v[240:241], v[140:141], v[248:249]
	v_pk_fma_f32 v[250:251], v[242:243], v[128:129], v[250:251]
	s_waitcnt vmcnt(23)
	v_cvt_f32_ubyte0_e32 v240, v200
	v_cvt_f32_ubyte1_e32 v241, v200
	v_cvt_f32_ubyte2_e32 v242, v200
	v_cvt_f32_ubyte3_e32 v243, v200
	v_pk_fma_f32 v[248:249], v[244:245], v[120:121], v[248:249]
	v_pk_fma_f32 v[250:251], v[246:247], v[112:113], v[250:251]
	v_cvt_f32_ubyte0_e32 v244, v201
	v_cvt_f32_ubyte1_e32 v245, v201
	v_cvt_f32_ubyte2_e32 v246, v201
	v_cvt_f32_ubyte3_e32 v247, v201
	v_pk_fma_f32 v[248:249], v[240:241], v[106:107], v[248:249]
	v_pk_fma_f32 v[250:251], v[242:243], v[102:103], v[250:251]
	v_cvt_f32_ubyte0_e32 v240, v202
	v_cvt_f32_ubyte1_e32 v241, v202
	v_cvt_f32_ubyte2_e32 v242, v202
	v_cvt_f32_ubyte3_e32 v243, v202
	v_pk_fma_f32 v[248:249], v[244:245], v[152:153], v[248:249]
	v_pk_fma_f32 v[250:251], v[246:247], v[100:101], v[250:251]
	v_cvt_f32_ubyte0_e32 v244, v203
	v_cvt_f32_ubyte1_e32 v245, v203
	v_cvt_f32_ubyte2_e32 v246, v203
	v_cvt_f32_ubyte3_e32 v247, v203
	global_load_dwordx4 v[200:203], v[194:195], off offset:1024
	v_pk_fma_f32 v[248:249], v[240:241], v[136:137], v[248:249]
	v_pk_fma_f32 v[250:251], v[242:243], v[122:123], v[250:251]
	s_waitcnt vmcnt(23)
	v_cvt_f32_ubyte0_e32 v240, v204
	v_cvt_f32_ubyte1_e32 v241, v204
	v_cvt_f32_ubyte2_e32 v242, v204
	v_cvt_f32_ubyte3_e32 v243, v204
	v_pk_fma_f32 v[248:249], v[244:245], v[116:117], v[248:249]
	v_pk_fma_f32 v[250:251], v[246:247], v[110:111], v[250:251]
	v_cvt_f32_ubyte0_e32 v244, v205
	v_cvt_f32_ubyte1_e32 v245, v205
	v_cvt_f32_ubyte2_e32 v246, v205
	v_cvt_f32_ubyte3_e32 v247, v205
	v_pk_fma_f32 v[248:249], v[240:241], v[156:157], v[248:249]
	v_pk_fma_f32 v[250:251], v[242:243], v[146:147], v[250:251]
	v_cvt_f32_ubyte0_e32 v240, v206
	v_cvt_f32_ubyte1_e32 v241, v206
	v_cvt_f32_ubyte2_e32 v242, v206
	v_cvt_f32_ubyte3_e32 v243, v206
	v_pk_fma_f32 v[248:249], v[244:245], v[142:143], v[248:249]
	v_pk_fma_f32 v[250:251], v[246:247], v[130:131], v[250:251]
	v_cvt_f32_ubyte0_e32 v244, v207
	v_cvt_f32_ubyte1_e32 v245, v207
	v_cvt_f32_ubyte2_e32 v246, v207
	v_cvt_f32_ubyte3_e32 v247, v207
	global_load_dwordx4 v[204:207], v[194:195], off offset:2048
	v_pk_fma_f32 v[248:249], v[240:241], v[124:125], v[248:249]
	v_pk_fma_f32 v[250:251], v[242:243], v[114:115], v[250:251]
	s_waitcnt vmcnt(23)
	v_cvt_f32_ubyte0_e32 v240, v208
	v_cvt_f32_ubyte1_e32 v241, v208
	v_cvt_f32_ubyte2_e32 v242, v208
	v_cvt_f32_ubyte3_e32 v243, v208
	v_pk_fma_f32 v[248:249], v[244:245], v[108:109], v[248:249]
	v_pk_fma_f32 v[250:251], v[246:247], v[104:105], v[250:251]
	v_cvt_f32_ubyte0_e32 v244, v209
	v_cvt_f32_ubyte1_e32 v245, v209
	v_cvt_f32_ubyte2_e32 v246, v209
	v_cvt_f32_ubyte3_e32 v247, v209
	v_pk_fma_f32 v[248:249], v[240:241], v[154:155], v[248:249]
	v_pk_fma_f32 v[250:251], v[242:243], v[138:139], v[250:251]
	v_cvt_f32_ubyte0_e32 v240, v210
	v_cvt_f32_ubyte1_e32 v241, v210
	v_cvt_f32_ubyte2_e32 v242, v210
	v_cvt_f32_ubyte3_e32 v243, v210
	v_pk_fma_f32 v[248:249], v[244:245], v[150:151], v[248:249]
	v_pk_fma_f32 v[250:251], v[246:247], v[132:133], v[250:251]
	v_cvt_f32_ubyte0_e32 v244, v211
	v_cvt_f32_ubyte1_e32 v245, v211
	v_cvt_f32_ubyte2_e32 v246, v211
	v_cvt_f32_ubyte3_e32 v247, v211
	global_load_dwordx4 v[208:211], v[194:195], off offset:3072
	v_pk_fma_f32 v[248:249], v[240:241], v[144:145], v[248:249]
	v_pk_fma_f32 v[250:251], v[242:243], v[126:127], v[250:251]
	v_readlane_b32 s30, v76, 11
	s_lshl_b32 s30, s30, 12
	v_lshl_add_u64 v[194:195], v[86:87], 0, s[30:31]
	s_waitcnt vmcnt(23)
	v_cvt_f32_ubyte0_e32 v240, v212
	v_cvt_f32_ubyte1_e32 v241, v212
	v_cvt_f32_ubyte2_e32 v242, v212
	v_cvt_f32_ubyte3_e32 v243, v212
	v_pk_fma_f32 v[248:249], v[244:245], v[134:135], v[248:249]
	v_pk_fma_f32 v[250:251], v[246:247], v[118:119], v[250:251]
	v_cvt_f32_ubyte0_e32 v244, v213
	v_cvt_f32_ubyte1_e32 v245, v213
	v_cvt_f32_ubyte2_e32 v246, v213
	v_cvt_f32_ubyte3_e32 v247, v213
	v_pk_add_f32 v[252:253], v[248:249], v[250:251]
	v_pk_mul_f32 v[248:249], v[240:241], v[162:163]
	v_pk_mul_f32 v[250:251], v[242:243], v[160:161]
	v_cvt_f32_ubyte0_e32 v240, v214
	v_cvt_f32_ubyte1_e32 v241, v214
	v_cvt_f32_ubyte2_e32 v242, v214
	v_cvt_f32_ubyte3_e32 v243, v214
	v_pk_fma_f32 v[248:249], v[244:245], v[158:159], v[248:249]
	v_pk_fma_f32 v[250:251], v[246:247], v[148:149], v[250:251]
	v_add_f32_e32 v182, v252, v253
	v_cvt_f32_ubyte0_e32 v244, v215
	v_cvt_f32_ubyte1_e32 v245, v215
	v_cvt_f32_ubyte2_e32 v246, v215
	v_cvt_f32_ubyte3_e32 v247, v215
	global_load_dwordx4 v[212:215], v[194:195], off
	v_pk_fma_f32 v[248:249], v[240:241], v[140:141], v[248:249]
	v_pk_fma_f32 v[250:251], v[242:243], v[128:129], v[250:251]
	s_waitcnt vmcnt(23)
	v_cvt_f32_ubyte0_e32 v240, v216
	v_cvt_f32_ubyte1_e32 v241, v216
	v_cvt_f32_ubyte2_e32 v242, v216
	v_cvt_f32_ubyte3_e32 v243, v216
	v_pk_fma_f32 v[248:249], v[244:245], v[120:121], v[248:249]
	v_pk_fma_f32 v[250:251], v[246:247], v[112:113], v[250:251]
	v_cvt_f32_ubyte0_e32 v244, v217
	v_cvt_f32_ubyte1_e32 v245, v217
	v_cvt_f32_ubyte2_e32 v246, v217
	v_cvt_f32_ubyte3_e32 v247, v217
	v_pk_fma_f32 v[248:249], v[240:241], v[106:107], v[248:249]
	v_pk_fma_f32 v[250:251], v[242:243], v[102:103], v[250:251]
	v_cvt_f32_ubyte0_e32 v240, v218
	v_cvt_f32_ubyte1_e32 v241, v218
	v_cvt_f32_ubyte2_e32 v242, v218
	v_cvt_f32_ubyte3_e32 v243, v218
	v_pk_fma_f32 v[248:249], v[244:245], v[152:153], v[248:249]
	v_pk_fma_f32 v[250:251], v[246:247], v[100:101], v[250:251]
	v_cvt_f32_ubyte0_e32 v244, v219
	v_cvt_f32_ubyte1_e32 v245, v219
	v_cvt_f32_ubyte2_e32 v246, v219
	v_cvt_f32_ubyte3_e32 v247, v219
	global_load_dwordx4 v[216:219], v[194:195], off offset:1024
	v_pk_fma_f32 v[248:249], v[240:241], v[136:137], v[248:249]
	v_pk_fma_f32 v[250:251], v[242:243], v[122:123], v[250:251]
	s_waitcnt vmcnt(23)
	v_cvt_f32_ubyte0_e32 v240, v220
	v_cvt_f32_ubyte1_e32 v241, v220
	v_cvt_f32_ubyte2_e32 v242, v220
	v_cvt_f32_ubyte3_e32 v243, v220
	v_pk_fma_f32 v[248:249], v[244:245], v[116:117], v[248:249]
	v_pk_fma_f32 v[250:251], v[246:247], v[110:111], v[250:251]
	v_cvt_f32_ubyte0_e32 v244, v221
	v_cvt_f32_ubyte1_e32 v245, v221
	v_cvt_f32_ubyte2_e32 v246, v221
	v_cvt_f32_ubyte3_e32 v247, v221
	v_pk_fma_f32 v[248:249], v[240:241], v[156:157], v[248:249]
	v_pk_fma_f32 v[250:251], v[242:243], v[146:147], v[250:251]
	v_cvt_f32_ubyte0_e32 v240, v222
	v_cvt_f32_ubyte1_e32 v241, v222
	v_cvt_f32_ubyte2_e32 v242, v222
	v_cvt_f32_ubyte3_e32 v243, v222
	v_pk_fma_f32 v[248:249], v[244:245], v[142:143], v[248:249]
	v_pk_fma_f32 v[250:251], v[246:247], v[130:131], v[250:251]
	v_cvt_f32_ubyte0_e32 v244, v223
	v_cvt_f32_ubyte1_e32 v245, v223
	v_cvt_f32_ubyte2_e32 v246, v223
	v_cvt_f32_ubyte3_e32 v247, v223
	global_load_dwordx4 v[220:223], v[194:195], off offset:2048
	v_pk_fma_f32 v[248:249], v[240:241], v[124:125], v[248:249]
	v_pk_fma_f32 v[250:251], v[242:243], v[114:115], v[250:251]
	s_waitcnt vmcnt(23)
	v_cvt_f32_ubyte0_e32 v240, v224
	v_cvt_f32_ubyte1_e32 v241, v224
	v_cvt_f32_ubyte2_e32 v242, v224
	v_cvt_f32_ubyte3_e32 v243, v224
	v_pk_fma_f32 v[248:249], v[244:245], v[108:109], v[248:249]
	v_pk_fma_f32 v[250:251], v[246:247], v[104:105], v[250:251]
	v_cvt_f32_ubyte0_e32 v244, v225
	v_cvt_f32_ubyte1_e32 v245, v225
	v_cvt_f32_ubyte2_e32 v246, v225
	v_cvt_f32_ubyte3_e32 v247, v225
	v_pk_fma_f32 v[248:249], v[240:241], v[154:155], v[248:249]
	v_pk_fma_f32 v[250:251], v[242:243], v[138:139], v[250:251]
	v_cvt_f32_ubyte0_e32 v240, v226
	v_cvt_f32_ubyte1_e32 v241, v226
	v_cvt_f32_ubyte2_e32 v242, v226
	v_cvt_f32_ubyte3_e32 v243, v226
	v_pk_fma_f32 v[248:249], v[244:245], v[150:151], v[248:249]
	v_pk_fma_f32 v[250:251], v[246:247], v[132:133], v[250:251]
	v_cvt_f32_ubyte0_e32 v244, v227
	v_cvt_f32_ubyte1_e32 v245, v227
	v_cvt_f32_ubyte2_e32 v246, v227
	v_cvt_f32_ubyte3_e32 v247, v227
	global_load_dwordx4 v[224:227], v[194:195], off offset:3072
	v_pk_fma_f32 v[248:249], v[240:241], v[144:145], v[248:249]
	v_pk_fma_f32 v[250:251], v[242:243], v[126:127], v[250:251]
	v_readlane_b32 s30, v76, 12
	s_lshl_b32 s30, s30, 12
	v_lshl_add_u64 v[194:195], v[86:87], 0, s[30:31]
	s_waitcnt vmcnt(23)
	v_cvt_f32_ubyte0_e32 v240, v10
	v_cvt_f32_ubyte1_e32 v241, v10
	v_cvt_f32_ubyte2_e32 v242, v10
	v_cvt_f32_ubyte3_e32 v243, v10
	v_pk_fma_f32 v[248:249], v[244:245], v[134:135], v[248:249]
	v_pk_fma_f32 v[250:251], v[246:247], v[118:119], v[250:251]
	v_cvt_f32_ubyte0_e32 v244, v11
	v_cvt_f32_ubyte1_e32 v245, v11
	v_cvt_f32_ubyte2_e32 v246, v11
	v_cvt_f32_ubyte3_e32 v247, v11
	v_pk_add_f32 v[252:253], v[248:249], v[250:251]
	v_pk_mul_f32 v[248:249], v[240:241], v[162:163]
	v_pk_mul_f32 v[250:251], v[242:243], v[160:161]
	v_cvt_f32_ubyte0_e32 v240, v12
	v_cvt_f32_ubyte1_e32 v241, v12
	v_cvt_f32_ubyte2_e32 v242, v12
	v_cvt_f32_ubyte3_e32 v243, v12
	v_pk_fma_f32 v[248:249], v[244:245], v[158:159], v[248:249]
	v_pk_fma_f32 v[250:251], v[246:247], v[148:149], v[250:251]
	v_add_f32_e32 v183, v252, v253
	v_cvt_f32_ubyte0_e32 v244, v13
	v_cvt_f32_ubyte1_e32 v245, v13
	v_cvt_f32_ubyte2_e32 v246, v13
	v_cvt_f32_ubyte3_e32 v247, v13
	global_load_dwordx4 v[10:13], v[194:195], off
	v_pk_fma_f32 v[248:249], v[240:241], v[140:141], v[248:249]
	v_pk_fma_f32 v[250:251], v[242:243], v[128:129], v[250:251]
	s_waitcnt vmcnt(23)
	v_cvt_f32_ubyte0_e32 v240, v14
	v_cvt_f32_ubyte1_e32 v241, v14
	v_cvt_f32_ubyte2_e32 v242, v14
	v_cvt_f32_ubyte3_e32 v243, v14
	v_pk_fma_f32 v[248:249], v[244:245], v[120:121], v[248:249]
	v_pk_fma_f32 v[250:251], v[246:247], v[112:113], v[250:251]
	v_cvt_f32_ubyte0_e32 v244, v15
	v_cvt_f32_ubyte1_e32 v245, v15
	v_cvt_f32_ubyte2_e32 v246, v15
	v_cvt_f32_ubyte3_e32 v247, v15
	v_pk_fma_f32 v[248:249], v[240:241], v[106:107], v[248:249]
	v_pk_fma_f32 v[250:251], v[242:243], v[102:103], v[250:251]
	v_cvt_f32_ubyte0_e32 v240, v16
	v_cvt_f32_ubyte1_e32 v241, v16
	v_cvt_f32_ubyte2_e32 v242, v16
	v_cvt_f32_ubyte3_e32 v243, v16
	v_pk_fma_f32 v[248:249], v[244:245], v[152:153], v[248:249]
	v_pk_fma_f32 v[250:251], v[246:247], v[100:101], v[250:251]
	v_cvt_f32_ubyte0_e32 v244, v17
	v_cvt_f32_ubyte1_e32 v245, v17
	v_cvt_f32_ubyte2_e32 v246, v17
	v_cvt_f32_ubyte3_e32 v247, v17
	global_load_dwordx4 v[14:17], v[194:195], off offset:1024
	v_pk_fma_f32 v[248:249], v[240:241], v[136:137], v[248:249]
	v_pk_fma_f32 v[250:251], v[242:243], v[122:123], v[250:251]
	s_waitcnt vmcnt(23)
	v_cvt_f32_ubyte0_e32 v240, v18
	v_cvt_f32_ubyte1_e32 v241, v18
	v_cvt_f32_ubyte2_e32 v242, v18
	v_cvt_f32_ubyte3_e32 v243, v18
	v_pk_fma_f32 v[248:249], v[244:245], v[116:117], v[248:249]
	v_pk_fma_f32 v[250:251], v[246:247], v[110:111], v[250:251]
	v_cvt_f32_ubyte0_e32 v244, v19
	v_cvt_f32_ubyte1_e32 v245, v19
	v_cvt_f32_ubyte2_e32 v246, v19
	v_cvt_f32_ubyte3_e32 v247, v19
	v_pk_fma_f32 v[248:249], v[240:241], v[156:157], v[248:249]
	v_pk_fma_f32 v[250:251], v[242:243], v[146:147], v[250:251]
	v_cvt_f32_ubyte0_e32 v240, v20
	v_cvt_f32_ubyte1_e32 v241, v20
	v_cvt_f32_ubyte2_e32 v242, v20
	v_cvt_f32_ubyte3_e32 v243, v20
	v_pk_fma_f32 v[248:249], v[244:245], v[142:143], v[248:249]
	v_pk_fma_f32 v[250:251], v[246:247], v[130:131], v[250:251]
	v_cvt_f32_ubyte0_e32 v244, v21
	v_cvt_f32_ubyte1_e32 v245, v21
	v_cvt_f32_ubyte2_e32 v246, v21
	v_cvt_f32_ubyte3_e32 v247, v21
	global_load_dwordx4 v[18:21], v[194:195], off offset:2048
	v_pk_fma_f32 v[248:249], v[240:241], v[124:125], v[248:249]
	v_pk_fma_f32 v[250:251], v[242:243], v[114:115], v[250:251]
	s_waitcnt vmcnt(23)
	v_cvt_f32_ubyte0_e32 v240, v22
	v_cvt_f32_ubyte1_e32 v241, v22
	v_cvt_f32_ubyte2_e32 v242, v22
	v_cvt_f32_ubyte3_e32 v243, v22
	v_pk_fma_f32 v[248:249], v[244:245], v[108:109], v[248:249]
	v_pk_fma_f32 v[250:251], v[246:247], v[104:105], v[250:251]
	v_cvt_f32_ubyte0_e32 v244, v23
	v_cvt_f32_ubyte1_e32 v245, v23
	v_cvt_f32_ubyte2_e32 v246, v23
	v_cvt_f32_ubyte3_e32 v247, v23
	v_pk_fma_f32 v[248:249], v[240:241], v[154:155], v[248:249]
	v_pk_fma_f32 v[250:251], v[242:243], v[138:139], v[250:251]
	v_cvt_f32_ubyte0_e32 v240, v24
	v_cvt_f32_ubyte1_e32 v241, v24
	v_cvt_f32_ubyte2_e32 v242, v24
	v_cvt_f32_ubyte3_e32 v243, v24
	v_pk_fma_f32 v[248:249], v[244:245], v[150:151], v[248:249]
	v_pk_fma_f32 v[250:251], v[246:247], v[132:133], v[250:251]
	v_cvt_f32_ubyte0_e32 v244, v25
	v_cvt_f32_ubyte1_e32 v245, v25
	v_cvt_f32_ubyte2_e32 v246, v25
	v_cvt_f32_ubyte3_e32 v247, v25
	global_load_dwordx4 v[22:25], v[194:195], off offset:3072
	v_pk_fma_f32 v[248:249], v[240:241], v[144:145], v[248:249]
	v_pk_fma_f32 v[250:251], v[242:243], v[126:127], v[250:251]
	v_readlane_b32 s30, v76, 13
	s_lshl_b32 s30, s30, 12
	v_lshl_add_u64 v[194:195], v[86:87], 0, s[30:31]
	s_waitcnt vmcnt(23)
	v_cvt_f32_ubyte0_e32 v240, v26
	v_cvt_f32_ubyte1_e32 v241, v26
	v_cvt_f32_ubyte2_e32 v242, v26
	v_cvt_f32_ubyte3_e32 v243, v26
	v_pk_fma_f32 v[248:249], v[244:245], v[134:135], v[248:249]
	v_pk_fma_f32 v[250:251], v[246:247], v[118:119], v[250:251]
	v_cvt_f32_ubyte0_e32 v244, v27
	v_cvt_f32_ubyte1_e32 v245, v27
	v_cvt_f32_ubyte2_e32 v246, v27
	v_cvt_f32_ubyte3_e32 v247, v27
	v_pk_add_f32 v[252:253], v[248:249], v[250:251]
	v_pk_mul_f32 v[248:249], v[240:241], v[162:163]
	v_pk_mul_f32 v[250:251], v[242:243], v[160:161]
	v_cvt_f32_ubyte0_e32 v240, v28
	v_cvt_f32_ubyte1_e32 v241, v28
	v_cvt_f32_ubyte2_e32 v242, v28
	v_cvt_f32_ubyte3_e32 v243, v28
	v_pk_fma_f32 v[248:249], v[244:245], v[158:159], v[248:249]
	v_pk_fma_f32 v[250:251], v[246:247], v[148:149], v[250:251]
	v_add_f32_e32 v184, v252, v253
	v_cvt_f32_ubyte0_e32 v244, v29
	v_cvt_f32_ubyte1_e32 v245, v29
	v_cvt_f32_ubyte2_e32 v246, v29
	v_cvt_f32_ubyte3_e32 v247, v29
	global_load_dwordx4 v[26:29], v[194:195], off
	v_pk_fma_f32 v[248:249], v[240:241], v[140:141], v[248:249]
	v_pk_fma_f32 v[250:251], v[242:243], v[128:129], v[250:251]
	s_waitcnt vmcnt(23)
	v_cvt_f32_ubyte0_e32 v240, v30
	v_cvt_f32_ubyte1_e32 v241, v30
	v_cvt_f32_ubyte2_e32 v242, v30
	v_cvt_f32_ubyte3_e32 v243, v30
	v_pk_fma_f32 v[248:249], v[244:245], v[120:121], v[248:249]
	v_pk_fma_f32 v[250:251], v[246:247], v[112:113], v[250:251]
	v_cvt_f32_ubyte0_e32 v244, v31
	v_cvt_f32_ubyte1_e32 v245, v31
	v_cvt_f32_ubyte2_e32 v246, v31
	v_cvt_f32_ubyte3_e32 v247, v31
	v_pk_fma_f32 v[248:249], v[240:241], v[106:107], v[248:249]
	v_pk_fma_f32 v[250:251], v[242:243], v[102:103], v[250:251]
	v_cvt_f32_ubyte0_e32 v240, v32
	v_cvt_f32_ubyte1_e32 v241, v32
	v_cvt_f32_ubyte2_e32 v242, v32
	v_cvt_f32_ubyte3_e32 v243, v32
	v_pk_fma_f32 v[248:249], v[244:245], v[152:153], v[248:249]
	v_pk_fma_f32 v[250:251], v[246:247], v[100:101], v[250:251]
	v_cvt_f32_ubyte0_e32 v244, v33
	v_cvt_f32_ubyte1_e32 v245, v33
	v_cvt_f32_ubyte2_e32 v246, v33
	v_cvt_f32_ubyte3_e32 v247, v33
	global_load_dwordx4 v[30:33], v[194:195], off offset:1024
	v_pk_fma_f32 v[248:249], v[240:241], v[136:137], v[248:249]
	v_pk_fma_f32 v[250:251], v[242:243], v[122:123], v[250:251]
	s_waitcnt vmcnt(23)
	v_cvt_f32_ubyte0_e32 v240, v34
	v_cvt_f32_ubyte1_e32 v241, v34
	v_cvt_f32_ubyte2_e32 v242, v34
	v_cvt_f32_ubyte3_e32 v243, v34
	v_pk_fma_f32 v[248:249], v[244:245], v[116:117], v[248:249]
	v_pk_fma_f32 v[250:251], v[246:247], v[110:111], v[250:251]
	v_cvt_f32_ubyte0_e32 v244, v35
	v_cvt_f32_ubyte1_e32 v245, v35
	v_cvt_f32_ubyte2_e32 v246, v35
	v_cvt_f32_ubyte3_e32 v247, v35
	v_pk_fma_f32 v[248:249], v[240:241], v[156:157], v[248:249]
	v_pk_fma_f32 v[250:251], v[242:243], v[146:147], v[250:251]
	v_cvt_f32_ubyte0_e32 v240, v36
	v_cvt_f32_ubyte1_e32 v241, v36
	v_cvt_f32_ubyte2_e32 v242, v36
	v_cvt_f32_ubyte3_e32 v243, v36
	v_pk_fma_f32 v[248:249], v[244:245], v[142:143], v[248:249]
	v_pk_fma_f32 v[250:251], v[246:247], v[130:131], v[250:251]
	v_cvt_f32_ubyte0_e32 v244, v37
	v_cvt_f32_ubyte1_e32 v245, v37
	v_cvt_f32_ubyte2_e32 v246, v37
	v_cvt_f32_ubyte3_e32 v247, v37
	global_load_dwordx4 v[34:37], v[194:195], off offset:2048
	v_pk_fma_f32 v[248:249], v[240:241], v[124:125], v[248:249]
	v_pk_fma_f32 v[250:251], v[242:243], v[114:115], v[250:251]
	s_waitcnt vmcnt(23)
	v_cvt_f32_ubyte0_e32 v240, v38
	v_cvt_f32_ubyte1_e32 v241, v38
	v_cvt_f32_ubyte2_e32 v242, v38
	v_cvt_f32_ubyte3_e32 v243, v38
	v_pk_fma_f32 v[248:249], v[244:245], v[108:109], v[248:249]
	v_pk_fma_f32 v[250:251], v[246:247], v[104:105], v[250:251]
	v_cvt_f32_ubyte0_e32 v244, v39
	v_cvt_f32_ubyte1_e32 v245, v39
	v_cvt_f32_ubyte2_e32 v246, v39
	v_cvt_f32_ubyte3_e32 v247, v39
	v_pk_fma_f32 v[248:249], v[240:241], v[154:155], v[248:249]
	v_pk_fma_f32 v[250:251], v[242:243], v[138:139], v[250:251]
	v_cvt_f32_ubyte0_e32 v240, v40
	v_cvt_f32_ubyte1_e32 v241, v40
	v_cvt_f32_ubyte2_e32 v242, v40
	v_cvt_f32_ubyte3_e32 v243, v40
	v_pk_fma_f32 v[248:249], v[244:245], v[150:151], v[248:249]
	v_pk_fma_f32 v[250:251], v[246:247], v[132:133], v[250:251]
	v_cvt_f32_ubyte0_e32 v244, v41
	v_cvt_f32_ubyte1_e32 v245, v41
	v_cvt_f32_ubyte2_e32 v246, v41
	v_cvt_f32_ubyte3_e32 v247, v41
	global_load_dwordx4 v[38:41], v[194:195], off offset:3072
	v_pk_fma_f32 v[248:249], v[240:241], v[144:145], v[248:249]
	v_pk_fma_f32 v[250:251], v[242:243], v[126:127], v[250:251]
	v_readlane_b32 s30, v76, 14
	s_lshl_b32 s30, s30, 12
	v_lshl_add_u64 v[194:195], v[86:87], 0, s[30:31]
	s_waitcnt vmcnt(23)
	v_cvt_f32_ubyte0_e32 v240, v42
	v_cvt_f32_ubyte1_e32 v241, v42
	v_cvt_f32_ubyte2_e32 v242, v42
	v_cvt_f32_ubyte3_e32 v243, v42
	v_pk_fma_f32 v[248:249], v[244:245], v[134:135], v[248:249]
	v_pk_fma_f32 v[250:251], v[246:247], v[118:119], v[250:251]
	v_cvt_f32_ubyte0_e32 v244, v43
	v_cvt_f32_ubyte1_e32 v245, v43
	v_cvt_f32_ubyte2_e32 v246, v43
	v_cvt_f32_ubyte3_e32 v247, v43
	v_pk_add_f32 v[252:253], v[248:249], v[250:251]
	v_pk_mul_f32 v[248:249], v[240:241], v[162:163]
	v_pk_mul_f32 v[250:251], v[242:243], v[160:161]
	v_cvt_f32_ubyte0_e32 v240, v44
	v_cvt_f32_ubyte1_e32 v241, v44
	v_cvt_f32_ubyte2_e32 v242, v44
	v_cvt_f32_ubyte3_e32 v243, v44
	v_pk_fma_f32 v[248:249], v[244:245], v[158:159], v[248:249]
	v_pk_fma_f32 v[250:251], v[246:247], v[148:149], v[250:251]
	v_add_f32_e32 v185, v252, v253
	v_cvt_f32_ubyte0_e32 v244, v45
	v_cvt_f32_ubyte1_e32 v245, v45
	v_cvt_f32_ubyte2_e32 v246, v45
	v_cvt_f32_ubyte3_e32 v247, v45
	global_load_dwordx4 v[42:45], v[194:195], off
	v_pk_fma_f32 v[248:249], v[240:241], v[140:141], v[248:249]
	v_pk_fma_f32 v[250:251], v[242:243], v[128:129], v[250:251]
	s_waitcnt vmcnt(23)
	v_cvt_f32_ubyte0_e32 v240, v46
	v_cvt_f32_ubyte1_e32 v241, v46
	v_cvt_f32_ubyte2_e32 v242, v46
	v_cvt_f32_ubyte3_e32 v243, v46
	v_pk_fma_f32 v[248:249], v[244:245], v[120:121], v[248:249]
	v_pk_fma_f32 v[250:251], v[246:247], v[112:113], v[250:251]
	v_cvt_f32_ubyte0_e32 v244, v47
	v_cvt_f32_ubyte1_e32 v245, v47
	v_cvt_f32_ubyte2_e32 v246, v47
	v_cvt_f32_ubyte3_e32 v247, v47
	v_pk_fma_f32 v[248:249], v[240:241], v[106:107], v[248:249]
	v_pk_fma_f32 v[250:251], v[242:243], v[102:103], v[250:251]
	v_cvt_f32_ubyte0_e32 v240, v48
	v_cvt_f32_ubyte1_e32 v241, v48
	v_cvt_f32_ubyte2_e32 v242, v48
	v_cvt_f32_ubyte3_e32 v243, v48
	v_pk_fma_f32 v[248:249], v[244:245], v[152:153], v[248:249]
	v_pk_fma_f32 v[250:251], v[246:247], v[100:101], v[250:251]
	v_cvt_f32_ubyte0_e32 v244, v49
	v_cvt_f32_ubyte1_e32 v245, v49
	v_cvt_f32_ubyte2_e32 v246, v49
	v_cvt_f32_ubyte3_e32 v247, v49
	global_load_dwordx4 v[46:49], v[194:195], off offset:1024
	v_pk_fma_f32 v[248:249], v[240:241], v[136:137], v[248:249]
	v_pk_fma_f32 v[250:251], v[242:243], v[122:123], v[250:251]
	s_waitcnt vmcnt(23)
	v_cvt_f32_ubyte0_e32 v240, v50
	v_cvt_f32_ubyte1_e32 v241, v50
	v_cvt_f32_ubyte2_e32 v242, v50
	v_cvt_f32_ubyte3_e32 v243, v50
	v_pk_fma_f32 v[248:249], v[244:245], v[116:117], v[248:249]
	v_pk_fma_f32 v[250:251], v[246:247], v[110:111], v[250:251]
	v_cvt_f32_ubyte0_e32 v244, v51
	v_cvt_f32_ubyte1_e32 v245, v51
	v_cvt_f32_ubyte2_e32 v246, v51
	v_cvt_f32_ubyte3_e32 v247, v51
	v_pk_fma_f32 v[248:249], v[240:241], v[156:157], v[248:249]
	v_pk_fma_f32 v[250:251], v[242:243], v[146:147], v[250:251]
	v_cvt_f32_ubyte0_e32 v240, v52
	v_cvt_f32_ubyte1_e32 v241, v52
	v_cvt_f32_ubyte2_e32 v242, v52
	v_cvt_f32_ubyte3_e32 v243, v52
	v_pk_fma_f32 v[248:249], v[244:245], v[142:143], v[248:249]
	v_pk_fma_f32 v[250:251], v[246:247], v[130:131], v[250:251]
	v_cvt_f32_ubyte0_e32 v244, v53
	v_cvt_f32_ubyte1_e32 v245, v53
	v_cvt_f32_ubyte2_e32 v246, v53
	v_cvt_f32_ubyte3_e32 v247, v53
	global_load_dwordx4 v[50:53], v[194:195], off offset:2048
	v_pk_fma_f32 v[248:249], v[240:241], v[124:125], v[248:249]
	v_pk_fma_f32 v[250:251], v[242:243], v[114:115], v[250:251]
	s_waitcnt vmcnt(23)
	v_cvt_f32_ubyte0_e32 v240, v54
	v_cvt_f32_ubyte1_e32 v241, v54
	v_cvt_f32_ubyte2_e32 v242, v54
	v_cvt_f32_ubyte3_e32 v243, v54
	v_pk_fma_f32 v[248:249], v[244:245], v[108:109], v[248:249]
	v_pk_fma_f32 v[250:251], v[246:247], v[104:105], v[250:251]
	v_cvt_f32_ubyte0_e32 v244, v55
	v_cvt_f32_ubyte1_e32 v245, v55
	v_cvt_f32_ubyte2_e32 v246, v55
	v_cvt_f32_ubyte3_e32 v247, v55
	v_pk_fma_f32 v[248:249], v[240:241], v[154:155], v[248:249]
	v_pk_fma_f32 v[250:251], v[242:243], v[138:139], v[250:251]
	v_cvt_f32_ubyte0_e32 v240, v56
	v_cvt_f32_ubyte1_e32 v241, v56
	v_cvt_f32_ubyte2_e32 v242, v56
	v_cvt_f32_ubyte3_e32 v243, v56
	v_pk_fma_f32 v[248:249], v[244:245], v[150:151], v[248:249]
	v_pk_fma_f32 v[250:251], v[246:247], v[132:133], v[250:251]
	v_cvt_f32_ubyte0_e32 v244, v57
	v_cvt_f32_ubyte1_e32 v245, v57
	v_cvt_f32_ubyte2_e32 v246, v57
	v_cvt_f32_ubyte3_e32 v247, v57
	global_load_dwordx4 v[54:57], v[194:195], off offset:3072
	v_pk_fma_f32 v[248:249], v[240:241], v[144:145], v[248:249]
	v_pk_fma_f32 v[250:251], v[242:243], v[126:127], v[250:251]
	v_readlane_b32 s30, v76, 15
	s_lshl_b32 s30, s30, 12
	v_lshl_add_u64 v[194:195], v[86:87], 0, s[30:31]
	s_waitcnt vmcnt(23)
	v_cvt_f32_ubyte0_e32 v240, v58
	v_cvt_f32_ubyte1_e32 v241, v58
	v_cvt_f32_ubyte2_e32 v242, v58
	v_cvt_f32_ubyte3_e32 v243, v58
	v_pk_fma_f32 v[248:249], v[244:245], v[134:135], v[248:249]
	v_pk_fma_f32 v[250:251], v[246:247], v[118:119], v[250:251]
	v_cvt_f32_ubyte0_e32 v244, v59
	v_cvt_f32_ubyte1_e32 v245, v59
	v_cvt_f32_ubyte2_e32 v246, v59
	v_cvt_f32_ubyte3_e32 v247, v59
	v_pk_add_f32 v[252:253], v[248:249], v[250:251]
	v_pk_mul_f32 v[248:249], v[240:241], v[162:163]
	v_pk_mul_f32 v[250:251], v[242:243], v[160:161]
	v_cvt_f32_ubyte0_e32 v240, v60
	v_cvt_f32_ubyte1_e32 v241, v60
	v_cvt_f32_ubyte2_e32 v242, v60
	v_cvt_f32_ubyte3_e32 v243, v60
	v_pk_fma_f32 v[248:249], v[244:245], v[158:159], v[248:249]
	v_pk_fma_f32 v[250:251], v[246:247], v[148:149], v[250:251]
	v_add_f32_e32 v186, v252, v253
	v_cvt_f32_ubyte0_e32 v244, v61
	v_cvt_f32_ubyte1_e32 v245, v61
	v_cvt_f32_ubyte2_e32 v246, v61
	v_cvt_f32_ubyte3_e32 v247, v61
	global_load_dwordx4 v[58:61], v[194:195], off
	v_pk_fma_f32 v[248:249], v[240:241], v[140:141], v[248:249]
	v_pk_fma_f32 v[250:251], v[242:243], v[128:129], v[250:251]
	s_waitcnt vmcnt(23)
	v_cvt_f32_ubyte0_e32 v240, v62
	v_cvt_f32_ubyte1_e32 v241, v62
	v_cvt_f32_ubyte2_e32 v242, v62
	v_cvt_f32_ubyte3_e32 v243, v62
	v_pk_fma_f32 v[248:249], v[244:245], v[120:121], v[248:249]
	v_pk_fma_f32 v[250:251], v[246:247], v[112:113], v[250:251]
	v_cvt_f32_ubyte0_e32 v244, v63
	v_cvt_f32_ubyte1_e32 v245, v63
	v_cvt_f32_ubyte2_e32 v246, v63
	v_cvt_f32_ubyte3_e32 v247, v63
	v_pk_fma_f32 v[248:249], v[240:241], v[106:107], v[248:249]
	v_pk_fma_f32 v[250:251], v[242:243], v[102:103], v[250:251]
	v_cvt_f32_ubyte0_e32 v240, v64
	v_cvt_f32_ubyte1_e32 v241, v64
	v_cvt_f32_ubyte2_e32 v242, v64
	v_cvt_f32_ubyte3_e32 v243, v64
	v_pk_fma_f32 v[248:249], v[244:245], v[152:153], v[248:249]
	v_pk_fma_f32 v[250:251], v[246:247], v[100:101], v[250:251]
	v_cvt_f32_ubyte0_e32 v244, v65
	v_cvt_f32_ubyte1_e32 v245, v65
	v_cvt_f32_ubyte2_e32 v246, v65
	v_cvt_f32_ubyte3_e32 v247, v65
	global_load_dwordx4 v[62:65], v[194:195], off offset:1024
	v_pk_fma_f32 v[248:249], v[240:241], v[136:137], v[248:249]
	v_pk_fma_f32 v[250:251], v[242:243], v[122:123], v[250:251]
	s_waitcnt vmcnt(23)
	v_cvt_f32_ubyte0_e32 v240, v66
	v_cvt_f32_ubyte1_e32 v241, v66
	v_cvt_f32_ubyte2_e32 v242, v66
	v_cvt_f32_ubyte3_e32 v243, v66
	v_pk_fma_f32 v[248:249], v[244:245], v[116:117], v[248:249]
	v_pk_fma_f32 v[250:251], v[246:247], v[110:111], v[250:251]
	v_cvt_f32_ubyte0_e32 v244, v67
	v_cvt_f32_ubyte1_e32 v245, v67
	v_cvt_f32_ubyte2_e32 v246, v67
	v_cvt_f32_ubyte3_e32 v247, v67
	v_pk_fma_f32 v[248:249], v[240:241], v[156:157], v[248:249]
	v_pk_fma_f32 v[250:251], v[242:243], v[146:147], v[250:251]
	v_cvt_f32_ubyte0_e32 v240, v68
	v_cvt_f32_ubyte1_e32 v241, v68
	v_cvt_f32_ubyte2_e32 v242, v68
	v_cvt_f32_ubyte3_e32 v243, v68
	v_pk_fma_f32 v[248:249], v[244:245], v[142:143], v[248:249]
	v_pk_fma_f32 v[250:251], v[246:247], v[130:131], v[250:251]
	v_cvt_f32_ubyte0_e32 v244, v69
	v_cvt_f32_ubyte1_e32 v245, v69
	v_cvt_f32_ubyte2_e32 v246, v69
	v_cvt_f32_ubyte3_e32 v247, v69
	global_load_dwordx4 v[66:69], v[194:195], off offset:2048
	v_pk_fma_f32 v[248:249], v[240:241], v[124:125], v[248:249]
	v_pk_fma_f32 v[250:251], v[242:243], v[114:115], v[250:251]
	s_waitcnt vmcnt(23)
	v_cvt_f32_ubyte0_e32 v240, v70
	v_cvt_f32_ubyte1_e32 v241, v70
	v_cvt_f32_ubyte2_e32 v242, v70
	v_cvt_f32_ubyte3_e32 v243, v70
	v_pk_fma_f32 v[248:249], v[244:245], v[108:109], v[248:249]
	v_pk_fma_f32 v[250:251], v[246:247], v[104:105], v[250:251]
	v_cvt_f32_ubyte0_e32 v244, v71
	v_cvt_f32_ubyte1_e32 v245, v71
	v_cvt_f32_ubyte2_e32 v246, v71
	v_cvt_f32_ubyte3_e32 v247, v71
	v_pk_fma_f32 v[248:249], v[240:241], v[154:155], v[248:249]
	v_pk_fma_f32 v[250:251], v[242:243], v[138:139], v[250:251]
	v_cvt_f32_ubyte0_e32 v240, v72
	v_cvt_f32_ubyte1_e32 v241, v72
	v_cvt_f32_ubyte2_e32 v242, v72
	v_cvt_f32_ubyte3_e32 v243, v72
	v_pk_fma_f32 v[248:249], v[244:245], v[150:151], v[248:249]
	v_pk_fma_f32 v[250:251], v[246:247], v[132:133], v[250:251]
	v_cvt_f32_ubyte0_e32 v244, v73
	v_cvt_f32_ubyte1_e32 v245, v73
	v_cvt_f32_ubyte2_e32 v246, v73
	v_cvt_f32_ubyte3_e32 v247, v73
	global_load_dwordx4 v[70:73], v[194:195], off offset:3072
	v_pk_fma_f32 v[248:249], v[240:241], v[144:145], v[248:249]
	v_pk_fma_f32 v[250:251], v[242:243], v[126:127], v[250:251]
	s_waitcnt vmcnt(23)
	v_cvt_f32_ubyte0_e32 v240, v196
	v_cvt_f32_ubyte1_e32 v241, v196
	v_cvt_f32_ubyte2_e32 v242, v196
	v_cvt_f32_ubyte3_e32 v243, v196
	v_pk_fma_f32 v[248:249], v[244:245], v[134:135], v[248:249]
	v_pk_fma_f32 v[250:251], v[246:247], v[118:119], v[250:251]
	v_cvt_f32_ubyte0_e32 v244, v197
	v_cvt_f32_ubyte1_e32 v245, v197
	v_cvt_f32_ubyte2_e32 v246, v197
	v_cvt_f32_ubyte3_e32 v247, v197
	v_pk_add_f32 v[252:253], v[248:249], v[250:251]
	v_pk_mul_f32 v[248:249], v[240:241], v[162:163]
	v_pk_mul_f32 v[250:251], v[242:243], v[160:161]
	v_cvt_f32_ubyte0_e32 v240, v198
	v_cvt_f32_ubyte1_e32 v241, v198
	v_cvt_f32_ubyte2_e32 v242, v198
	v_cvt_f32_ubyte3_e32 v243, v198
	v_pk_fma_f32 v[248:249], v[244:245], v[158:159], v[248:249]
	v_pk_fma_f32 v[250:251], v[246:247], v[148:149], v[250:251]
	v_add_f32_e32 v187, v252, v253
	v_cvt_f32_ubyte0_e32 v244, v199
	v_cvt_f32_ubyte1_e32 v245, v199
	v_cvt_f32_ubyte2_e32 v246, v199
	v_cvt_f32_ubyte3_e32 v247, v199
	v_pk_fma_f32 v[248:249], v[240:241], v[140:141], v[248:249]
	v_pk_fma_f32 v[250:251], v[242:243], v[128:129], v[250:251]
	s_waitcnt vmcnt(22)
	v_cvt_f32_ubyte0_e32 v240, v200
	v_cvt_f32_ubyte1_e32 v241, v200
	v_cvt_f32_ubyte2_e32 v242, v200
	v_cvt_f32_ubyte3_e32 v243, v200
	v_pk_fma_f32 v[248:249], v[244:245], v[120:121], v[248:249]
	v_pk_fma_f32 v[250:251], v[246:247], v[112:113], v[250:251]
	v_cvt_f32_ubyte0_e32 v244, v201
	v_cvt_f32_ubyte1_e32 v245, v201
	v_cvt_f32_ubyte2_e32 v246, v201
	v_cvt_f32_ubyte3_e32 v247, v201
	v_pk_fma_f32 v[248:249], v[240:241], v[106:107], v[248:249]
	v_pk_fma_f32 v[250:251], v[242:243], v[102:103], v[250:251]
	v_cvt_f32_ubyte0_e32 v240, v202
	v_cvt_f32_ubyte1_e32 v241, v202
	v_cvt_f32_ubyte2_e32 v242, v202
	v_cvt_f32_ubyte3_e32 v243, v202
	v_pk_fma_f32 v[248:249], v[244:245], v[152:153], v[248:249]
	v_pk_fma_f32 v[250:251], v[246:247], v[100:101], v[250:251]
	v_cvt_f32_ubyte0_e32 v244, v203
	v_cvt_f32_ubyte1_e32 v245, v203
	v_cvt_f32_ubyte2_e32 v246, v203
	v_cvt_f32_ubyte3_e32 v247, v203
	v_pk_fma_f32 v[248:249], v[240:241], v[136:137], v[248:249]
	v_pk_fma_f32 v[250:251], v[242:243], v[122:123], v[250:251]
	s_waitcnt vmcnt(21)
	v_cvt_f32_ubyte0_e32 v240, v204
	v_cvt_f32_ubyte1_e32 v241, v204
	v_cvt_f32_ubyte2_e32 v242, v204
	v_cvt_f32_ubyte3_e32 v243, v204
	v_pk_fma_f32 v[248:249], v[244:245], v[116:117], v[248:249]
	v_pk_fma_f32 v[250:251], v[246:247], v[110:111], v[250:251]
	v_cvt_f32_ubyte0_e32 v244, v205
	v_cvt_f32_ubyte1_e32 v245, v205
	v_cvt_f32_ubyte2_e32 v246, v205
	v_cvt_f32_ubyte3_e32 v247, v205
	v_pk_fma_f32 v[248:249], v[240:241], v[156:157], v[248:249]
	v_pk_fma_f32 v[250:251], v[242:243], v[146:147], v[250:251]
	v_cvt_f32_ubyte0_e32 v240, v206
	v_cvt_f32_ubyte1_e32 v241, v206
	v_cvt_f32_ubyte2_e32 v242, v206
	v_cvt_f32_ubyte3_e32 v243, v206
	v_pk_fma_f32 v[248:249], v[244:245], v[142:143], v[248:249]
	v_pk_fma_f32 v[250:251], v[246:247], v[130:131], v[250:251]
	v_cvt_f32_ubyte0_e32 v244, v207
	v_cvt_f32_ubyte1_e32 v245, v207
	v_cvt_f32_ubyte2_e32 v246, v207
	v_cvt_f32_ubyte3_e32 v247, v207
	v_pk_fma_f32 v[248:249], v[240:241], v[124:125], v[248:249]
	v_pk_fma_f32 v[250:251], v[242:243], v[114:115], v[250:251]
	s_waitcnt vmcnt(20)
	v_cvt_f32_ubyte0_e32 v240, v208
	v_cvt_f32_ubyte1_e32 v241, v208
	v_cvt_f32_ubyte2_e32 v242, v208
	v_cvt_f32_ubyte3_e32 v243, v208
	v_pk_fma_f32 v[248:249], v[244:245], v[108:109], v[248:249]
	v_pk_fma_f32 v[250:251], v[246:247], v[104:105], v[250:251]
	v_cvt_f32_ubyte0_e32 v244, v209
	v_cvt_f32_ubyte1_e32 v245, v209
	v_cvt_f32_ubyte2_e32 v246, v209
	v_cvt_f32_ubyte3_e32 v247, v209
	v_pk_fma_f32 v[248:249], v[240:241], v[154:155], v[248:249]
	v_pk_fma_f32 v[250:251], v[242:243], v[138:139], v[250:251]
	v_cvt_f32_ubyte0_e32 v240, v210
	v_cvt_f32_ubyte1_e32 v241, v210
	v_cvt_f32_ubyte2_e32 v242, v210
	v_cvt_f32_ubyte3_e32 v243, v210
	v_pk_fma_f32 v[248:249], v[244:245], v[150:151], v[248:249]
	v_pk_fma_f32 v[250:251], v[246:247], v[132:133], v[250:251]
	v_cvt_f32_ubyte0_e32 v244, v211
	v_cvt_f32_ubyte1_e32 v245, v211
	v_cvt_f32_ubyte2_e32 v246, v211
	v_cvt_f32_ubyte3_e32 v247, v211
	v_pk_fma_f32 v[248:249], v[240:241], v[144:145], v[248:249]
	v_pk_fma_f32 v[250:251], v[242:243], v[126:127], v[250:251]
	s_waitcnt vmcnt(19)
	v_cvt_f32_ubyte0_e32 v240, v212
	v_cvt_f32_ubyte1_e32 v241, v212
	v_cvt_f32_ubyte2_e32 v242, v212
	v_cvt_f32_ubyte3_e32 v243, v212
	v_pk_fma_f32 v[248:249], v[244:245], v[134:135], v[248:249]
	v_pk_fma_f32 v[250:251], v[246:247], v[118:119], v[250:251]
	v_cvt_f32_ubyte0_e32 v244, v213
	v_cvt_f32_ubyte1_e32 v245, v213
	v_cvt_f32_ubyte2_e32 v246, v213
	v_cvt_f32_ubyte3_e32 v247, v213
	v_pk_add_f32 v[252:253], v[248:249], v[250:251]
	v_pk_mul_f32 v[248:249], v[240:241], v[162:163]
	v_pk_mul_f32 v[250:251], v[242:243], v[160:161]
	v_cvt_f32_ubyte0_e32 v240, v214
	v_cvt_f32_ubyte1_e32 v241, v214
	v_cvt_f32_ubyte2_e32 v242, v214
	v_cvt_f32_ubyte3_e32 v243, v214
	v_pk_fma_f32 v[248:249], v[244:245], v[158:159], v[248:249]
	v_pk_fma_f32 v[250:251], v[246:247], v[148:149], v[250:251]
	v_add_f32_e32 v188, v252, v253
	v_cvt_f32_ubyte0_e32 v244, v215
	v_cvt_f32_ubyte1_e32 v245, v215
	v_cvt_f32_ubyte2_e32 v246, v215
	v_cvt_f32_ubyte3_e32 v247, v215
	v_pk_fma_f32 v[248:249], v[240:241], v[140:141], v[248:249]
	v_pk_fma_f32 v[250:251], v[242:243], v[128:129], v[250:251]
	s_waitcnt vmcnt(18)
	v_cvt_f32_ubyte0_e32 v240, v216
	v_cvt_f32_ubyte1_e32 v241, v216
	v_cvt_f32_ubyte2_e32 v242, v216
	v_cvt_f32_ubyte3_e32 v243, v216
	v_pk_fma_f32 v[248:249], v[244:245], v[120:121], v[248:249]
	v_pk_fma_f32 v[250:251], v[246:247], v[112:113], v[250:251]
	v_cvt_f32_ubyte0_e32 v244, v217
	v_cvt_f32_ubyte1_e32 v245, v217
	v_cvt_f32_ubyte2_e32 v246, v217
	v_cvt_f32_ubyte3_e32 v247, v217
	v_pk_fma_f32 v[248:249], v[240:241], v[106:107], v[248:249]
	v_pk_fma_f32 v[250:251], v[242:243], v[102:103], v[250:251]
	v_cvt_f32_ubyte0_e32 v240, v218
	v_cvt_f32_ubyte1_e32 v241, v218
	v_cvt_f32_ubyte2_e32 v242, v218
	v_cvt_f32_ubyte3_e32 v243, v218
	v_pk_fma_f32 v[248:249], v[244:245], v[152:153], v[248:249]
	v_pk_fma_f32 v[250:251], v[246:247], v[100:101], v[250:251]
	v_cvt_f32_ubyte0_e32 v244, v219
	v_cvt_f32_ubyte1_e32 v245, v219
	v_cvt_f32_ubyte2_e32 v246, v219
	v_cvt_f32_ubyte3_e32 v247, v219
	v_pk_fma_f32 v[248:249], v[240:241], v[136:137], v[248:249]
	v_pk_fma_f32 v[250:251], v[242:243], v[122:123], v[250:251]
	s_waitcnt vmcnt(17)
	v_cvt_f32_ubyte0_e32 v240, v220
	v_cvt_f32_ubyte1_e32 v241, v220
	v_cvt_f32_ubyte2_e32 v242, v220
	v_cvt_f32_ubyte3_e32 v243, v220
	v_pk_fma_f32 v[248:249], v[244:245], v[116:117], v[248:249]
	v_pk_fma_f32 v[250:251], v[246:247], v[110:111], v[250:251]
	v_cvt_f32_ubyte0_e32 v244, v221
	v_cvt_f32_ubyte1_e32 v245, v221
	v_cvt_f32_ubyte2_e32 v246, v221
	v_cvt_f32_ubyte3_e32 v247, v221
	v_pk_fma_f32 v[248:249], v[240:241], v[156:157], v[248:249]
	v_pk_fma_f32 v[250:251], v[242:243], v[146:147], v[250:251]
	v_cvt_f32_ubyte0_e32 v240, v222
	v_cvt_f32_ubyte1_e32 v241, v222
	v_cvt_f32_ubyte2_e32 v242, v222
	v_cvt_f32_ubyte3_e32 v243, v222
	v_pk_fma_f32 v[248:249], v[244:245], v[142:143], v[248:249]
	v_pk_fma_f32 v[250:251], v[246:247], v[130:131], v[250:251]
	v_cvt_f32_ubyte0_e32 v244, v223
	v_cvt_f32_ubyte1_e32 v245, v223
	v_cvt_f32_ubyte2_e32 v246, v223
	v_cvt_f32_ubyte3_e32 v247, v223
	v_pk_fma_f32 v[248:249], v[240:241], v[124:125], v[248:249]
	v_pk_fma_f32 v[250:251], v[242:243], v[114:115], v[250:251]
	s_waitcnt vmcnt(16)
	v_cvt_f32_ubyte0_e32 v240, v224
	v_cvt_f32_ubyte1_e32 v241, v224
	v_cvt_f32_ubyte2_e32 v242, v224
	v_cvt_f32_ubyte3_e32 v243, v224
	v_pk_fma_f32 v[248:249], v[244:245], v[108:109], v[248:249]
	v_pk_fma_f32 v[250:251], v[246:247], v[104:105], v[250:251]
	v_cvt_f32_ubyte0_e32 v244, v225
	v_cvt_f32_ubyte1_e32 v245, v225
	v_cvt_f32_ubyte2_e32 v246, v225
	v_cvt_f32_ubyte3_e32 v247, v225
	v_pk_fma_f32 v[248:249], v[240:241], v[154:155], v[248:249]
	v_pk_fma_f32 v[250:251], v[242:243], v[138:139], v[250:251]
	v_cvt_f32_ubyte0_e32 v240, v226
	v_cvt_f32_ubyte1_e32 v241, v226
	v_cvt_f32_ubyte2_e32 v242, v226
	v_cvt_f32_ubyte3_e32 v243, v226
	v_pk_fma_f32 v[248:249], v[244:245], v[150:151], v[248:249]
	v_pk_fma_f32 v[250:251], v[246:247], v[132:133], v[250:251]
	v_cvt_f32_ubyte0_e32 v244, v227
	v_cvt_f32_ubyte1_e32 v245, v227
	v_cvt_f32_ubyte2_e32 v246, v227
	v_cvt_f32_ubyte3_e32 v247, v227
	v_pk_fma_f32 v[248:249], v[240:241], v[144:145], v[248:249]
	v_pk_fma_f32 v[250:251], v[242:243], v[126:127], v[250:251]
	s_waitcnt vmcnt(15)
	v_cvt_f32_ubyte0_e32 v240, v10
	v_cvt_f32_ubyte1_e32 v241, v10
	v_cvt_f32_ubyte2_e32 v242, v10
	v_cvt_f32_ubyte3_e32 v243, v10
	v_pk_fma_f32 v[248:249], v[244:245], v[134:135], v[248:249]
	v_pk_fma_f32 v[250:251], v[246:247], v[118:119], v[250:251]
	v_cvt_f32_ubyte0_e32 v244, v11
	v_cvt_f32_ubyte1_e32 v245, v11
	v_cvt_f32_ubyte2_e32 v246, v11
	v_cvt_f32_ubyte3_e32 v247, v11
	v_pk_add_f32 v[252:253], v[248:249], v[250:251]
	v_pk_mul_f32 v[248:249], v[240:241], v[162:163]
	v_pk_mul_f32 v[250:251], v[242:243], v[160:161]
	v_cvt_f32_ubyte0_e32 v240, v12
	v_cvt_f32_ubyte1_e32 v241, v12
	v_cvt_f32_ubyte2_e32 v242, v12
	v_cvt_f32_ubyte3_e32 v243, v12
	v_pk_fma_f32 v[248:249], v[244:245], v[158:159], v[248:249]
	v_pk_fma_f32 v[250:251], v[246:247], v[148:149], v[250:251]
	v_add_f32_e32 v189, v252, v253
	v_cvt_f32_ubyte0_e32 v244, v13
	v_cvt_f32_ubyte1_e32 v245, v13
	v_cvt_f32_ubyte2_e32 v246, v13
	v_cvt_f32_ubyte3_e32 v247, v13
	v_pk_fma_f32 v[248:249], v[240:241], v[140:141], v[248:249]
	v_pk_fma_f32 v[250:251], v[242:243], v[128:129], v[250:251]
	s_waitcnt vmcnt(14)
	v_cvt_f32_ubyte0_e32 v240, v14
	v_cvt_f32_ubyte1_e32 v241, v14
	v_cvt_f32_ubyte2_e32 v242, v14
	v_cvt_f32_ubyte3_e32 v243, v14
	v_pk_fma_f32 v[248:249], v[244:245], v[120:121], v[248:249]
	v_pk_fma_f32 v[250:251], v[246:247], v[112:113], v[250:251]
	v_cvt_f32_ubyte0_e32 v244, v15
	v_cvt_f32_ubyte1_e32 v245, v15
	v_cvt_f32_ubyte2_e32 v246, v15
	v_cvt_f32_ubyte3_e32 v247, v15
	v_pk_fma_f32 v[248:249], v[240:241], v[106:107], v[248:249]
	v_pk_fma_f32 v[250:251], v[242:243], v[102:103], v[250:251]
	v_cvt_f32_ubyte0_e32 v240, v16
	v_cvt_f32_ubyte1_e32 v241, v16
	v_cvt_f32_ubyte2_e32 v242, v16
	v_cvt_f32_ubyte3_e32 v243, v16
	v_pk_fma_f32 v[248:249], v[244:245], v[152:153], v[248:249]
	v_pk_fma_f32 v[250:251], v[246:247], v[100:101], v[250:251]
	v_cvt_f32_ubyte0_e32 v244, v17
	v_cvt_f32_ubyte1_e32 v245, v17
	v_cvt_f32_ubyte2_e32 v246, v17
	v_cvt_f32_ubyte3_e32 v247, v17
	v_pk_fma_f32 v[248:249], v[240:241], v[136:137], v[248:249]
	v_pk_fma_f32 v[250:251], v[242:243], v[122:123], v[250:251]
	s_waitcnt vmcnt(13)
	v_cvt_f32_ubyte0_e32 v240, v18
	v_cvt_f32_ubyte1_e32 v241, v18
	v_cvt_f32_ubyte2_e32 v242, v18
	v_cvt_f32_ubyte3_e32 v243, v18
	v_pk_fma_f32 v[248:249], v[244:245], v[116:117], v[248:249]
	v_pk_fma_f32 v[250:251], v[246:247], v[110:111], v[250:251]
	v_cvt_f32_ubyte0_e32 v244, v19
	v_cvt_f32_ubyte1_e32 v245, v19
	v_cvt_f32_ubyte2_e32 v246, v19
	v_cvt_f32_ubyte3_e32 v247, v19
	v_pk_fma_f32 v[248:249], v[240:241], v[156:157], v[248:249]
	v_pk_fma_f32 v[250:251], v[242:243], v[146:147], v[250:251]
	v_cvt_f32_ubyte0_e32 v240, v20
	v_cvt_f32_ubyte1_e32 v241, v20
	v_cvt_f32_ubyte2_e32 v242, v20
	v_cvt_f32_ubyte3_e32 v243, v20
	v_pk_fma_f32 v[248:249], v[244:245], v[142:143], v[248:249]
	v_pk_fma_f32 v[250:251], v[246:247], v[130:131], v[250:251]
	v_cvt_f32_ubyte0_e32 v244, v21
	v_cvt_f32_ubyte1_e32 v245, v21
	v_cvt_f32_ubyte2_e32 v246, v21
	v_cvt_f32_ubyte3_e32 v247, v21
	v_pk_fma_f32 v[248:249], v[240:241], v[124:125], v[248:249]
	v_pk_fma_f32 v[250:251], v[242:243], v[114:115], v[250:251]
	s_waitcnt vmcnt(12)
	v_cvt_f32_ubyte0_e32 v240, v22
	v_cvt_f32_ubyte1_e32 v241, v22
	v_cvt_f32_ubyte2_e32 v242, v22
	v_cvt_f32_ubyte3_e32 v243, v22
	v_pk_fma_f32 v[248:249], v[244:245], v[108:109], v[248:249]
	v_pk_fma_f32 v[250:251], v[246:247], v[104:105], v[250:251]
	v_cvt_f32_ubyte0_e32 v244, v23
	v_cvt_f32_ubyte1_e32 v245, v23
	v_cvt_f32_ubyte2_e32 v246, v23
	v_cvt_f32_ubyte3_e32 v247, v23
	v_pk_fma_f32 v[248:249], v[240:241], v[154:155], v[248:249]
	v_pk_fma_f32 v[250:251], v[242:243], v[138:139], v[250:251]
	v_cvt_f32_ubyte0_e32 v240, v24
	v_cvt_f32_ubyte1_e32 v241, v24
	v_cvt_f32_ubyte2_e32 v242, v24
	v_cvt_f32_ubyte3_e32 v243, v24
	v_pk_fma_f32 v[248:249], v[244:245], v[150:151], v[248:249]
	v_pk_fma_f32 v[250:251], v[246:247], v[132:133], v[250:251]
	v_cvt_f32_ubyte0_e32 v244, v25
	v_cvt_f32_ubyte1_e32 v245, v25
	v_cvt_f32_ubyte2_e32 v246, v25
	v_cvt_f32_ubyte3_e32 v247, v25
	v_pk_fma_f32 v[248:249], v[240:241], v[144:145], v[248:249]
	v_pk_fma_f32 v[250:251], v[242:243], v[126:127], v[250:251]
	s_waitcnt vmcnt(11)
	v_cvt_f32_ubyte0_e32 v240, v26
	v_cvt_f32_ubyte1_e32 v241, v26
	v_cvt_f32_ubyte2_e32 v242, v26
	v_cvt_f32_ubyte3_e32 v243, v26
	v_pk_fma_f32 v[248:249], v[244:245], v[134:135], v[248:249]
	v_pk_fma_f32 v[250:251], v[246:247], v[118:119], v[250:251]
	v_cvt_f32_ubyte0_e32 v244, v27
	v_cvt_f32_ubyte1_e32 v245, v27
	v_cvt_f32_ubyte2_e32 v246, v27
	v_cvt_f32_ubyte3_e32 v247, v27
	v_pk_add_f32 v[252:253], v[248:249], v[250:251]
	v_pk_mul_f32 v[248:249], v[240:241], v[162:163]
	v_pk_mul_f32 v[250:251], v[242:243], v[160:161]
	v_cvt_f32_ubyte0_e32 v240, v28
	v_cvt_f32_ubyte1_e32 v241, v28
	v_cvt_f32_ubyte2_e32 v242, v28
	v_cvt_f32_ubyte3_e32 v243, v28
	v_pk_fma_f32 v[248:249], v[244:245], v[158:159], v[248:249]
	v_pk_fma_f32 v[250:251], v[246:247], v[148:149], v[250:251]
	v_add_f32_e32 v190, v252, v253
	v_cvt_f32_ubyte0_e32 v244, v29
	v_cvt_f32_ubyte1_e32 v245, v29
	v_cvt_f32_ubyte2_e32 v246, v29
	v_cvt_f32_ubyte3_e32 v247, v29
	v_pk_fma_f32 v[248:249], v[240:241], v[140:141], v[248:249]
	v_pk_fma_f32 v[250:251], v[242:243], v[128:129], v[250:251]
	s_waitcnt vmcnt(10)
	v_cvt_f32_ubyte0_e32 v240, v30
	v_cvt_f32_ubyte1_e32 v241, v30
	v_cvt_f32_ubyte2_e32 v242, v30
	v_cvt_f32_ubyte3_e32 v243, v30
	v_pk_fma_f32 v[248:249], v[244:245], v[120:121], v[248:249]
	v_pk_fma_f32 v[250:251], v[246:247], v[112:113], v[250:251]
	v_cvt_f32_ubyte0_e32 v244, v31
	v_cvt_f32_ubyte1_e32 v245, v31
	v_cvt_f32_ubyte2_e32 v246, v31
	v_cvt_f32_ubyte3_e32 v247, v31
	v_pk_fma_f32 v[248:249], v[240:241], v[106:107], v[248:249]
	v_pk_fma_f32 v[250:251], v[242:243], v[102:103], v[250:251]
	v_cvt_f32_ubyte0_e32 v240, v32
	v_cvt_f32_ubyte1_e32 v241, v32
	v_cvt_f32_ubyte2_e32 v242, v32
	v_cvt_f32_ubyte3_e32 v243, v32
	v_pk_fma_f32 v[248:249], v[244:245], v[152:153], v[248:249]
	v_pk_fma_f32 v[250:251], v[246:247], v[100:101], v[250:251]
	v_cvt_f32_ubyte0_e32 v244, v33
	v_cvt_f32_ubyte1_e32 v245, v33
	v_cvt_f32_ubyte2_e32 v246, v33
	v_cvt_f32_ubyte3_e32 v247, v33
	v_pk_fma_f32 v[248:249], v[240:241], v[136:137], v[248:249]
	v_pk_fma_f32 v[250:251], v[242:243], v[122:123], v[250:251]
	s_waitcnt vmcnt(9)
	v_cvt_f32_ubyte0_e32 v240, v34
	v_cvt_f32_ubyte1_e32 v241, v34
	v_cvt_f32_ubyte2_e32 v242, v34
	v_cvt_f32_ubyte3_e32 v243, v34
	v_pk_fma_f32 v[248:249], v[244:245], v[116:117], v[248:249]
	v_pk_fma_f32 v[250:251], v[246:247], v[110:111], v[250:251]
	v_cvt_f32_ubyte0_e32 v244, v35
	v_cvt_f32_ubyte1_e32 v245, v35
	v_cvt_f32_ubyte2_e32 v246, v35
	v_cvt_f32_ubyte3_e32 v247, v35
	v_pk_fma_f32 v[248:249], v[240:241], v[156:157], v[248:249]
	v_pk_fma_f32 v[250:251], v[242:243], v[146:147], v[250:251]
	v_cvt_f32_ubyte0_e32 v240, v36
	v_cvt_f32_ubyte1_e32 v241, v36
	v_cvt_f32_ubyte2_e32 v242, v36
	v_cvt_f32_ubyte3_e32 v243, v36
	v_pk_fma_f32 v[248:249], v[244:245], v[142:143], v[248:249]
	v_pk_fma_f32 v[250:251], v[246:247], v[130:131], v[250:251]
	v_cvt_f32_ubyte0_e32 v244, v37
	v_cvt_f32_ubyte1_e32 v245, v37
	v_cvt_f32_ubyte2_e32 v246, v37
	v_cvt_f32_ubyte3_e32 v247, v37
	v_pk_fma_f32 v[248:249], v[240:241], v[124:125], v[248:249]
	v_pk_fma_f32 v[250:251], v[242:243], v[114:115], v[250:251]
	s_waitcnt vmcnt(8)
	v_cvt_f32_ubyte0_e32 v240, v38
	v_cvt_f32_ubyte1_e32 v241, v38
	v_cvt_f32_ubyte2_e32 v242, v38
	v_cvt_f32_ubyte3_e32 v243, v38
	v_pk_fma_f32 v[248:249], v[244:245], v[108:109], v[248:249]
	v_pk_fma_f32 v[250:251], v[246:247], v[104:105], v[250:251]
	v_cvt_f32_ubyte0_e32 v244, v39
	v_cvt_f32_ubyte1_e32 v245, v39
	v_cvt_f32_ubyte2_e32 v246, v39
	v_cvt_f32_ubyte3_e32 v247, v39
	v_pk_fma_f32 v[248:249], v[240:241], v[154:155], v[248:249]
	v_pk_fma_f32 v[250:251], v[242:243], v[138:139], v[250:251]
	v_cvt_f32_ubyte0_e32 v240, v40
	v_cvt_f32_ubyte1_e32 v241, v40
	v_cvt_f32_ubyte2_e32 v242, v40
	v_cvt_f32_ubyte3_e32 v243, v40
	v_pk_fma_f32 v[248:249], v[244:245], v[150:151], v[248:249]
	v_pk_fma_f32 v[250:251], v[246:247], v[132:133], v[250:251]
	v_cvt_f32_ubyte0_e32 v244, v41
	v_cvt_f32_ubyte1_e32 v245, v41
	v_cvt_f32_ubyte2_e32 v246, v41
	v_cvt_f32_ubyte3_e32 v247, v41
	v_pk_fma_f32 v[248:249], v[240:241], v[144:145], v[248:249]
	v_pk_fma_f32 v[250:251], v[242:243], v[126:127], v[250:251]
	s_waitcnt vmcnt(7)
	v_cvt_f32_ubyte0_e32 v240, v42
	v_cvt_f32_ubyte1_e32 v241, v42
	v_cvt_f32_ubyte2_e32 v242, v42
	v_cvt_f32_ubyte3_e32 v243, v42
	v_pk_fma_f32 v[248:249], v[244:245], v[134:135], v[248:249]
	v_pk_fma_f32 v[250:251], v[246:247], v[118:119], v[250:251]
	v_cvt_f32_ubyte0_e32 v244, v43
	v_cvt_f32_ubyte1_e32 v245, v43
	v_cvt_f32_ubyte2_e32 v246, v43
	v_cvt_f32_ubyte3_e32 v247, v43
	v_pk_add_f32 v[252:253], v[248:249], v[250:251]
	v_pk_mul_f32 v[248:249], v[240:241], v[162:163]
	v_pk_mul_f32 v[250:251], v[242:243], v[160:161]
	v_cvt_f32_ubyte0_e32 v240, v44
	v_cvt_f32_ubyte1_e32 v241, v44
	v_cvt_f32_ubyte2_e32 v242, v44
	v_cvt_f32_ubyte3_e32 v243, v44
	v_pk_fma_f32 v[248:249], v[244:245], v[158:159], v[248:249]
	v_pk_fma_f32 v[250:251], v[246:247], v[148:149], v[250:251]
	v_add_f32_e32 v191, v252, v253
	v_cvt_f32_ubyte0_e32 v244, v45
	v_cvt_f32_ubyte1_e32 v245, v45
	v_cvt_f32_ubyte2_e32 v246, v45
	v_cvt_f32_ubyte3_e32 v247, v45
	v_pk_fma_f32 v[248:249], v[240:241], v[140:141], v[248:249]
	v_pk_fma_f32 v[250:251], v[242:243], v[128:129], v[250:251]
	s_waitcnt vmcnt(6)
	v_cvt_f32_ubyte0_e32 v240, v46
	v_cvt_f32_ubyte1_e32 v241, v46
	v_cvt_f32_ubyte2_e32 v242, v46
	v_cvt_f32_ubyte3_e32 v243, v46
	v_pk_fma_f32 v[248:249], v[244:245], v[120:121], v[248:249]
	v_pk_fma_f32 v[250:251], v[246:247], v[112:113], v[250:251]
	v_cvt_f32_ubyte0_e32 v244, v47
	v_cvt_f32_ubyte1_e32 v245, v47
	v_cvt_f32_ubyte2_e32 v246, v47
	v_cvt_f32_ubyte3_e32 v247, v47
	v_pk_fma_f32 v[248:249], v[240:241], v[106:107], v[248:249]
	v_pk_fma_f32 v[250:251], v[242:243], v[102:103], v[250:251]
	v_cvt_f32_ubyte0_e32 v240, v48
	v_cvt_f32_ubyte1_e32 v241, v48
	v_cvt_f32_ubyte2_e32 v242, v48
	v_cvt_f32_ubyte3_e32 v243, v48
	v_pk_fma_f32 v[248:249], v[244:245], v[152:153], v[248:249]
	v_pk_fma_f32 v[250:251], v[246:247], v[100:101], v[250:251]
	v_cvt_f32_ubyte0_e32 v244, v49
	v_cvt_f32_ubyte1_e32 v245, v49
	v_cvt_f32_ubyte2_e32 v246, v49
	v_cvt_f32_ubyte3_e32 v247, v49
	v_pk_fma_f32 v[248:249], v[240:241], v[136:137], v[248:249]
	v_pk_fma_f32 v[250:251], v[242:243], v[122:123], v[250:251]
	s_waitcnt vmcnt(5)
	v_cvt_f32_ubyte0_e32 v240, v50
	v_cvt_f32_ubyte1_e32 v241, v50
	v_cvt_f32_ubyte2_e32 v242, v50
	v_cvt_f32_ubyte3_e32 v243, v50
	v_pk_fma_f32 v[248:249], v[244:245], v[116:117], v[248:249]
	v_pk_fma_f32 v[250:251], v[246:247], v[110:111], v[250:251]
	v_cvt_f32_ubyte0_e32 v244, v51
	v_cvt_f32_ubyte1_e32 v245, v51
	v_cvt_f32_ubyte2_e32 v246, v51
	v_cvt_f32_ubyte3_e32 v247, v51
	v_pk_fma_f32 v[248:249], v[240:241], v[156:157], v[248:249]
	v_pk_fma_f32 v[250:251], v[242:243], v[146:147], v[250:251]
	v_cvt_f32_ubyte0_e32 v240, v52
	v_cvt_f32_ubyte1_e32 v241, v52
	v_cvt_f32_ubyte2_e32 v242, v52
	v_cvt_f32_ubyte3_e32 v243, v52
	v_pk_fma_f32 v[248:249], v[244:245], v[142:143], v[248:249]
	v_pk_fma_f32 v[250:251], v[246:247], v[130:131], v[250:251]
	v_cvt_f32_ubyte0_e32 v244, v53
	v_cvt_f32_ubyte1_e32 v245, v53
	v_cvt_f32_ubyte2_e32 v246, v53
	v_cvt_f32_ubyte3_e32 v247, v53
	v_pk_fma_f32 v[248:249], v[240:241], v[124:125], v[248:249]
	v_pk_fma_f32 v[250:251], v[242:243], v[114:115], v[250:251]
	s_waitcnt vmcnt(4)
	v_cvt_f32_ubyte0_e32 v240, v54
	v_cvt_f32_ubyte1_e32 v241, v54
	v_cvt_f32_ubyte2_e32 v242, v54
	v_cvt_f32_ubyte3_e32 v243, v54
	v_pk_fma_f32 v[248:249], v[244:245], v[108:109], v[248:249]
	v_pk_fma_f32 v[250:251], v[246:247], v[104:105], v[250:251]
	v_cvt_f32_ubyte0_e32 v244, v55
	v_cvt_f32_ubyte1_e32 v245, v55
	v_cvt_f32_ubyte2_e32 v246, v55
	v_cvt_f32_ubyte3_e32 v247, v55
	v_pk_fma_f32 v[248:249], v[240:241], v[154:155], v[248:249]
	v_pk_fma_f32 v[250:251], v[242:243], v[138:139], v[250:251]
	v_cvt_f32_ubyte0_e32 v240, v56
	v_cvt_f32_ubyte1_e32 v241, v56
	v_cvt_f32_ubyte2_e32 v242, v56
	v_cvt_f32_ubyte3_e32 v243, v56
	v_pk_fma_f32 v[248:249], v[244:245], v[150:151], v[248:249]
	v_pk_fma_f32 v[250:251], v[246:247], v[132:133], v[250:251]
	v_cvt_f32_ubyte0_e32 v244, v57
	v_cvt_f32_ubyte1_e32 v245, v57
	v_cvt_f32_ubyte2_e32 v246, v57
	v_cvt_f32_ubyte3_e32 v247, v57
	v_pk_fma_f32 v[248:249], v[240:241], v[144:145], v[248:249]
	v_pk_fma_f32 v[250:251], v[242:243], v[126:127], v[250:251]
	s_waitcnt vmcnt(3)
	v_cvt_f32_ubyte0_e32 v240, v58
	v_cvt_f32_ubyte1_e32 v241, v58
	v_cvt_f32_ubyte2_e32 v242, v58
	v_cvt_f32_ubyte3_e32 v243, v58
	v_pk_fma_f32 v[248:249], v[244:245], v[134:135], v[248:249]
	v_pk_fma_f32 v[250:251], v[246:247], v[118:119], v[250:251]
	v_cvt_f32_ubyte0_e32 v244, v59
	v_cvt_f32_ubyte1_e32 v245, v59
	v_cvt_f32_ubyte2_e32 v246, v59
	v_cvt_f32_ubyte3_e32 v247, v59
	v_pk_add_f32 v[252:253], v[248:249], v[250:251]
	v_pk_mul_f32 v[248:249], v[240:241], v[162:163]
	v_pk_mul_f32 v[250:251], v[242:243], v[160:161]
	v_cvt_f32_ubyte0_e32 v240, v60
	v_cvt_f32_ubyte1_e32 v241, v60
	v_cvt_f32_ubyte2_e32 v242, v60
	v_cvt_f32_ubyte3_e32 v243, v60
	v_pk_fma_f32 v[248:249], v[244:245], v[158:159], v[248:249]
	v_pk_fma_f32 v[250:251], v[246:247], v[148:149], v[250:251]
	v_add_f32_e32 v192, v252, v253
	v_cvt_f32_ubyte0_e32 v244, v61
	v_cvt_f32_ubyte1_e32 v245, v61
	v_cvt_f32_ubyte2_e32 v246, v61
	v_cvt_f32_ubyte3_e32 v247, v61
	v_pk_fma_f32 v[248:249], v[240:241], v[140:141], v[248:249]
	v_pk_fma_f32 v[250:251], v[242:243], v[128:129], v[250:251]
	s_waitcnt vmcnt(2)
	v_cvt_f32_ubyte0_e32 v240, v62
	v_cvt_f32_ubyte1_e32 v241, v62
	v_cvt_f32_ubyte2_e32 v242, v62
	v_cvt_f32_ubyte3_e32 v243, v62
	v_pk_fma_f32 v[248:249], v[244:245], v[120:121], v[248:249]
	v_pk_fma_f32 v[250:251], v[246:247], v[112:113], v[250:251]
	v_cvt_f32_ubyte0_e32 v244, v63
	v_cvt_f32_ubyte1_e32 v245, v63
	v_cvt_f32_ubyte2_e32 v246, v63
	v_cvt_f32_ubyte3_e32 v247, v63
	v_pk_fma_f32 v[248:249], v[240:241], v[106:107], v[248:249]
	v_pk_fma_f32 v[250:251], v[242:243], v[102:103], v[250:251]
	v_cvt_f32_ubyte0_e32 v240, v64
	v_cvt_f32_ubyte1_e32 v241, v64
	v_cvt_f32_ubyte2_e32 v242, v64
	v_cvt_f32_ubyte3_e32 v243, v64
	v_pk_fma_f32 v[248:249], v[244:245], v[152:153], v[248:249]
	v_pk_fma_f32 v[250:251], v[246:247], v[100:101], v[250:251]
	v_cvt_f32_ubyte0_e32 v244, v65
	v_cvt_f32_ubyte1_e32 v245, v65
	v_cvt_f32_ubyte2_e32 v246, v65
	v_cvt_f32_ubyte3_e32 v247, v65
	v_pk_fma_f32 v[248:249], v[240:241], v[136:137], v[248:249]
	v_pk_fma_f32 v[250:251], v[242:243], v[122:123], v[250:251]
	s_waitcnt vmcnt(1)
	v_cvt_f32_ubyte0_e32 v240, v66
	v_cvt_f32_ubyte1_e32 v241, v66
	v_cvt_f32_ubyte2_e32 v242, v66
	v_cvt_f32_ubyte3_e32 v243, v66
	v_pk_fma_f32 v[248:249], v[244:245], v[116:117], v[248:249]
	v_pk_fma_f32 v[250:251], v[246:247], v[110:111], v[250:251]
	v_cvt_f32_ubyte0_e32 v244, v67
	v_cvt_f32_ubyte1_e32 v245, v67
	v_cvt_f32_ubyte2_e32 v246, v67
	v_cvt_f32_ubyte3_e32 v247, v67
	v_pk_fma_f32 v[248:249], v[240:241], v[156:157], v[248:249]
	v_pk_fma_f32 v[250:251], v[242:243], v[146:147], v[250:251]
	v_cvt_f32_ubyte0_e32 v240, v68
	v_cvt_f32_ubyte1_e32 v241, v68
	v_cvt_f32_ubyte2_e32 v242, v68
	v_cvt_f32_ubyte3_e32 v243, v68
	v_pk_fma_f32 v[248:249], v[244:245], v[142:143], v[248:249]
	v_pk_fma_f32 v[250:251], v[246:247], v[130:131], v[250:251]
	v_cvt_f32_ubyte0_e32 v244, v69
	v_cvt_f32_ubyte1_e32 v245, v69
	v_cvt_f32_ubyte2_e32 v246, v69
	v_cvt_f32_ubyte3_e32 v247, v69
	v_pk_fma_f32 v[248:249], v[240:241], v[124:125], v[248:249]
	v_pk_fma_f32 v[250:251], v[242:243], v[114:115], v[250:251]
	s_waitcnt vmcnt(0)
	v_cvt_f32_ubyte0_e32 v240, v70
	v_cvt_f32_ubyte1_e32 v241, v70
	v_cvt_f32_ubyte2_e32 v242, v70
	v_cvt_f32_ubyte3_e32 v243, v70
	v_pk_fma_f32 v[248:249], v[244:245], v[108:109], v[248:249]
	v_pk_fma_f32 v[250:251], v[246:247], v[104:105], v[250:251]
	v_cvt_f32_ubyte0_e32 v244, v71
	v_cvt_f32_ubyte1_e32 v245, v71
	v_cvt_f32_ubyte2_e32 v246, v71
	v_cvt_f32_ubyte3_e32 v247, v71
	v_pk_fma_f32 v[248:249], v[240:241], v[154:155], v[248:249]
	v_pk_fma_f32 v[250:251], v[242:243], v[138:139], v[250:251]
	v_cvt_f32_ubyte0_e32 v240, v72
	v_cvt_f32_ubyte1_e32 v241, v72
	v_cvt_f32_ubyte2_e32 v242, v72
	v_cvt_f32_ubyte3_e32 v243, v72
	v_pk_fma_f32 v[248:249], v[244:245], v[150:151], v[248:249]
	v_pk_fma_f32 v[250:251], v[246:247], v[132:133], v[250:251]
	v_cvt_f32_ubyte0_e32 v244, v73
	v_cvt_f32_ubyte1_e32 v245, v73
	v_cvt_f32_ubyte2_e32 v246, v73
	v_cvt_f32_ubyte3_e32 v247, v73
	v_pk_fma_f32 v[248:249], v[240:241], v[144:145], v[248:249]
	v_pk_fma_f32 v[250:251], v[242:243], v[126:127], v[250:251]
	v_pk_fma_f32 v[248:249], v[244:245], v[134:135], v[248:249]
	v_pk_fma_f32 v[250:251], v[246:247], v[118:119], v[250:251]
	v_pk_add_f32 v[252:253], v[248:249], v[250:251]
	v_mov_b32_e32 v14, v190
	v_mov_b32_e32 v15, v191
	v_mov_b32_e32 v16, v192
	v_add_f32_e32 v10, v252, v253
	v_cndmask_b32_e64 v12, v178, v186, s[4:5]
	ds_bpermute_b32 v12, v170, v12
	v_cndmask_b32_e64 v13, v179, v187, s[4:5]
	ds_bpermute_b32 v13, v170, v13
	v_cndmask_b32_e64 v17, v180, v188, s[4:5]
	ds_bpermute_b32 v17, v170, v17
	v_cndmask_b32_e64 v18, v181, v189, s[4:5]
	v_cndmask_b32_e64 v19, v182, v14, s[4:5]
	ds_bpermute_b32 v18, v170, v18
	ds_bpermute_b32 v19, v170, v19
	v_cndmask_b32_e64 v11, v186, v178, s[4:5]
	s_waitcnt lgkmcnt(4)
	v_add_f32_e32 v11, v11, v12
	v_cndmask_b32_e64 v12, v187, v179, s[4:5]
	s_waitcnt lgkmcnt(3)
	v_add_f32_e32 v12, v12, v13
	v_cndmask_b32_e64 v13, v188, v180, s[4:5]
	s_waitcnt lgkmcnt(2)
	v_add_f32_e32 v13, v13, v17
	v_cndmask_b32_e64 v17, v189, v181, s[4:5]
	v_cndmask_b32_e64 v14, v14, v182, s[4:5]
	v_cndmask_b32_e64 v20, v183, v15, s[4:5]
	s_waitcnt lgkmcnt(1)
	v_add_f32_e32 v17, v17, v18
	s_waitcnt lgkmcnt(0)
	v_add_f32_e32 v14, v14, v19
	v_cndmask_b32_e64 v18, v16, v184, s[4:5]
	v_cndmask_b32_e64 v16, v184, v16, s[4:5]
	v_cndmask_b32_e64 v19, v185, v10, s[4:5]
	ds_bpermute_b32 v20, v170, v20
	ds_bpermute_b32 v16, v170, v16
	ds_bpermute_b32 v19, v170, v19
	v_cndmask_b32_e64 v15, v15, v183, s[4:5]
	v_cndmask_b32_e64 v10, v10, v185, s[4:5]
	s_waitcnt lgkmcnt(2)
	v_add_f32_e32 v15, v15, v20
	s_waitcnt lgkmcnt(1)
	v_add_f32_e32 v16, v18, v16
	s_waitcnt lgkmcnt(0)
	v_add_f32_e32 v10, v10, v19
	v_cndmask_b32_e64 v20, v11, v14, s[6:7]
	v_cndmask_b32_e64 v11, v14, v11, s[6:7]
	v_cndmask_b32_e64 v14, v15, v12, s[6:7]
	v_cndmask_b32_e64 v12, v12, v15, s[6:7]
	v_cndmask_b32_e64 v15, v13, v16, s[6:7]
	v_cndmask_b32_e64 v18, v17, v10, s[6:7]
	ds_bpermute_b32 v20, v169, v20
	ds_bpermute_b32 v12, v169, v12
	ds_bpermute_b32 v15, v169, v15
	ds_bpermute_b32 v18, v169, v18
	v_cndmask_b32_e64 v13, v16, v13, s[6:7]
	v_cndmask_b32_e64 v10, v10, v17, s[6:7]
	s_waitcnt lgkmcnt(3)
	v_add_f32_e32 v11, v11, v20
	s_waitcnt lgkmcnt(2)
	v_add_f32_e32 v12, v14, v12
	s_waitcnt lgkmcnt(1)
	v_add_f32_e32 v13, v13, v15
	s_waitcnt lgkmcnt(0)
	v_add_f32_e32 v10, v10, v18
	v_cndmask_b32_e64 v14, v11, v13, s[8:9]
	v_cndmask_b32_e64 v15, v12, v10, s[8:9]
	ds_bpermute_b32 v14, v168, v14
	ds_bpermute_b32 v15, v168, v15
	v_cndmask_b32_e64 v11, v13, v11, s[8:9]
	v_cndmask_b32_e64 v10, v10, v12, s[8:9]
	s_waitcnt lgkmcnt(1)
	v_add_f32_e32 v11, v11, v14
	s_waitcnt lgkmcnt(0)
	v_add_f32_e32 v10, v10, v15
	v_cndmask_b32_e64 v12, v11, v10, s[10:11]
	ds_bpermute_b32 v12, v167, v12
	v_cndmask_b32_e64 v10, v10, v11, s[10:11]
	s_waitcnt lgkmcnt(0)
	v_add_f32_e32 v10, v10, v12
	ds_bpermute_b32 v11, v166, v10
	s_waitcnt lgkmcnt(0)
	v_add_f32_e32 v10, v10, v11
	ds_bpermute_b32 v11, v165, v10
	s_waitcnt lgkmcnt(0)
	v_add_f32_e32 v10, v10, v11
	ds_bpermute_b32 v11, v80, v10
	v_mov_b32_e32 v10, 0
	s_and_saveexec_b64 s[30:31], s[2:3]
	s_cbranch_execz .LBB0_1479
	v_add_f32_e32 v99, v99, v177
	v_pk_mul_f32 v[12:13], v[98:99], v[96:97]
	s_waitcnt lgkmcnt(0)
	v_sub_f32_e32 v10, v11, v13
	v_mul_f32_e32 v10, v12, v10
	v_mul_f32_e32 v11, 0x3f3504f3, v10
	v_cmp_nlt_f32_e64 s[34:35], |v11|, 1.0
	s_and_saveexec_b64 s[52:53], s[34:35]
	s_xor_b64 s[34:35], exec, s[52:53]
	s_cbranch_execz .LBB0_1476
	v_fma_f32 v12, |v11|, s41, v175
	v_fma_f32 v12, |v11|, v12, s42
	v_fma_f32 v12, |v11|, v12, s43
	v_fma_f32 v12, |v11|, v12, s44
	v_fma_f32 v12, |v11|, v12, s45
	v_fma_f32 v12, |v11|, v12, s46
	v_fma_f32 v12, |v11|, v12, |v11|
	v_mul_f32_e32 v13, 0xbfb8aa3b, v12
	v_fma_f32 v14, v12, s47, -v13
	v_rndne_f32_e32 v15, v13
	v_fmac_f32_e32 v14, 0xb2a5705f, v12
	v_sub_f32_e32 v13, v13, v15
	v_add_f32_e32 v13, v13, v14
	v_cvt_i32_f32_e32 v14, v15
	v_exp_f32_e32 v13, v13
	v_cmp_nlt_f32_e32 vcc, s48, v12
	v_ldexp_f32 v13, v13, v14
	s_nop 0
	v_cndmask_b32_e32 v13, 0, v13, vcc
	v_cmp_ngt_f32_e32 vcc, s49, v12
	s_nop 1
	v_cndmask_b32_e32 v12, v176, v13, vcc
	v_sub_f32_e32 v12, 1.0, v12
